# v_Y plus 46 LDS-DMA loads of the P2/P10/P12/P15 K-loops in SGPR-base + 32-bit VGPR-offset form (64-bit VALU address adds dropped where the temporary is dead)
# baseline (speedup 1.0000x reference)
.LBB0_318:
	ds_read_b128 v[26:29], v185
	ds_read_b128 v[30:33], v185 offset:1024
	ds_read_b128 v[18:21], v185 offset:2048
	ds_read_b128 v[22:25], v185 offset:3072
	ds_read_b128 v[10:13], v186
	ds_read_b128 v[14:17], v186 offset:1024
	ds_read_b128 v[2:5], v186 offset:2048
	ds_read_b128 v[6:9], v186 offset:3072
	s_add_u32 s24, s26, 0xffea8080
	s_addc_u32 s25, s27, -1
	s_cmpk_eq_i32 s58, 0x52
	s_cselect_b32 s31, s5, s25
	s_cselect_b32 s30, s4, s24
	s_cselect_b32 s29, s21, s51
	s_cselect_b32 s28, s20, s50
	s_add_i32 m0, s7, 0xc000
	ds_read_b128 v[174:177], v187
	ds_read_b128 v[178:181], v187 offset:1024
	ds_read_b128 v[188:191], v187 offset:2048
	ds_read_b128 v[192:195], v187 offset:3072
	ds_read_b128 v[196:199], v187 offset:4096
	ds_read_b128 v[200:203], v187 offset:5120
	ds_read_b128 v[204:207], v187 offset:6144
	ds_read_b128 v[208:211], v187 offset:7168
	global_load_lds_dwordx4 v166, s[26:27]
	v_lshl_add_u64 v[212:213], s[26:27], 0, v[168:169]
	s_add_i32 m0, s7, 0xe000
	s_nop 0
	global_load_lds_dwordx4 v[212:213], off
	s_waitcnt vmcnt(8)
	s_waitcnt lgkmcnt(0)
	s_barrier
	s_setprio 1
	v_mfma_f32_16x16x128_f8f6f4 v[158:161], v[26:33], v[174:181], v[158:161]
	v_mfma_f32_16x16x128_f8f6f4 v[154:157], v[18:25], v[174:181], v[154:157]
	v_mfma_f32_16x16x128_f8f6f4 v[138:141], v[18:25], v[188:195], v[138:141]
	v_mfma_f32_16x16x128_f8f6f4 v[142:145], v[26:33], v[188:195], v[142:145]
	v_mfma_f32_16x16x128_f8f6f4 v[126:129], v[26:33], v[196:203], v[126:129]
	v_mfma_f32_16x16x128_f8f6f4 v[122:125], v[18:25], v[196:203], v[122:125]
	v_mfma_f32_16x16x128_f8f6f4 v[106:109], v[18:25], v[204:211], v[106:109]
	v_mfma_f32_16x16x128_f8f6f4 v[110:113], v[26:33], v[204:211], v[110:113]
	v_mfma_f32_16x16x128_f8f6f4 v[102:105], v[10:17], v[204:211], v[102:105]
	v_mfma_f32_16x16x128_f8f6f4 v[98:101], v[2:9], v[204:211], v[98:101]
	v_mfma_f32_16x16x128_f8f6f4 v[146:149], v[2:9], v[174:181], v[146:149]
	v_mfma_f32_16x16x128_f8f6f4 v[150:153], v[10:17], v[174:181], v[150:153]
	v_mfma_f32_16x16x128_f8f6f4 v[134:137], v[10:17], v[188:195], v[134:137]
	v_mfma_f32_16x16x128_f8f6f4 v[130:133], v[2:9], v[188:195], v[130:133]
	v_mfma_f32_16x16x128_f8f6f4 v[114:117], v[2:9], v[196:203], v[114:117]
	v_mfma_f32_16x16x128_f8f6f4 v[118:121], v[10:17], v[196:203], v[118:121]
	s_setprio 0
	s_barrier
	s_add_i32 s24, s42, s3
	v_lshl_add_u64 v[174:175], s[28:29], 0, v[164:165]
	s_mov_b32 m0, s24
	ds_read_b128 v[188:191], v187 offset:16384
	ds_read_b128 v[192:195], v187 offset:17408
	ds_read_b128 v[196:199], v187 offset:18432
	ds_read_b128 v[200:203], v187 offset:19456
	ds_read_b128 v[204:207], v187 offset:20480
	ds_read_b128 v[208:211], v187 offset:21504
	ds_read_b128 v[212:215], v187 offset:22528
	ds_read_b128 v[216:219], v187 offset:23552
	global_load_lds_dwordx4 v[174:175], off
	s_add_i32 m0, s24, 0x2000
	s_add_u32 s24, s28, 0x158000
	v_lshl_add_u64 v[176:177], s[28:29], 0, v[162:163]
	s_addc_u32 s25, s29, 0
	s_add_i32 s59, s43, s3
	global_load_lds_dwordx4 v[176:177], off
	s_mov_b32 m0, s59
	v_lshl_add_u64 v[180:181], s[30:31], 0, v[162:163]
	global_load_lds_dwordx4 v164, s[24:25]
	s_add_i32 m0, s59, 0x2000
	s_nop 0
	global_load_lds_dwordx4 v162, s[24:25]
	v_lshl_add_u64 v[178:179], s[30:31], 0, v[164:165]
	s_mov_b32 m0, s7
	s_nop 0
	global_load_lds_dwordx4 v[178:179], off
	s_mov_b32 m0, s17
	s_nop 0
	global_load_lds_dwordx4 v[180:181], off
	s_waitcnt vmcnt(8)
	s_waitcnt lgkmcnt(0)
	s_barrier
	s_setprio 1
	v_mfma_f32_16x16x128_f8f6f4 v[78:81], v[26:33], v[196:203], v[78:81]
	v_mfma_f32_16x16x128_f8f6f4 v[74:77], v[18:25], v[196:203], v[74:77]
	v_mfma_f32_16x16x128_f8f6f4 v[90:93], v[18:25], v[188:195], v[90:93]
	v_mfma_f32_16x16x128_f8f6f4 v[94:97], v[26:33], v[188:195], v[94:97]
	v_mfma_f32_16x16x128_f8f6f4 v[62:65], v[26:33], v[204:211], v[62:65]
	v_mfma_f32_16x16x128_f8f6f4 v[58:61], v[18:25], v[204:211], v[58:61]
	v_mfma_f32_16x16x128_f8f6f4 v[42:45], v[18:25], v[212:219], v[42:45]
	v_mfma_f32_16x16x128_f8f6f4 v[46:49], v[26:33], v[212:219], v[46:49]
	v_mfma_f32_16x16x128_f8f6f4 v[38:41], v[10:17], v[212:219], v[38:41]
	v_mfma_f32_16x16x128_f8f6f4 v[34:37], v[2:9], v[212:219], v[34:37]
	v_mfma_f32_16x16x128_f8f6f4 v[82:85], v[2:9], v[188:195], v[82:85]
	v_mfma_f32_16x16x128_f8f6f4 v[86:89], v[10:17], v[188:195], v[86:89]
	v_mfma_f32_16x16x128_f8f6f4 v[70:73], v[10:17], v[196:203], v[70:73]
	v_mfma_f32_16x16x128_f8f6f4 v[66:69], v[2:9], v[196:203], v[66:69]
	v_mfma_f32_16x16x128_f8f6f4 v[50:53], v[2:9], v[204:211], v[50:53]
	v_mfma_f32_16x16x128_f8f6f4 v[54:57], v[10:17], v[204:211], v[54:57]
	s_setprio 0
	s_barrier
	s_add_i32 s59, 0, 0x18000
	s_add_i32 s60, 0, 0x1c000
	v_add_u32_e32 v14, s59, v183
	v_add_u32_e32 v30, s60, v183
	ds_read_b128 v[2:5], v14
	ds_read_b128 v[6:9], v14 offset:1024
	ds_read_b128 v[10:13], v14 offset:2048
	ds_read_b128 v[14:17], v14 offset:3072
	ds_read_b128 v[18:21], v30
	ds_read_b128 v[22:25], v30 offset:1024
	ds_read_b128 v[26:29], v30 offset:2048
	ds_read_b128 v[30:33], v30 offset:3072
	s_add_u32 s24, s30, 0x158000
	s_addc_u32 s25, s31, 0
	s_mov_b32 m0, s34
	ds_read_b128 v[188:191], v187 offset:32768
	ds_read_b128 v[192:195], v187 offset:33792
	ds_read_b128 v[196:199], v187 offset:34816
	ds_read_b128 v[200:203], v187 offset:35840
	ds_read_b128 v[204:207], v187 offset:36864
	ds_read_b128 v[208:211], v187 offset:37888
	ds_read_b128 v[212:215], v187 offset:38912
	ds_read_b128 v[216:219], v187 offset:39936
	global_load_lds_dwordx4 v164, s[24:25]
	s_mov_b32 m0, s35
	s_nop 0
	global_load_lds_dwordx4 v162, s[24:25]
	s_waitcnt vmcnt(8)
	s_waitcnt lgkmcnt(0)
	s_barrier
	s_setprio 1
	v_mfma_f32_16x16x128_f8f6f4 v[122:125], v[10:17], v[204:211], v[122:125]
	v_mfma_f32_16x16x128_f8f6f4 v[126:129], v[2:9], v[204:211], v[126:129]
	v_mfma_f32_16x16x128_f8f6f4 v[158:161], v[2:9], v[188:195], v[158:161]
	v_mfma_f32_16x16x128_f8f6f4 v[154:157], v[10:17], v[188:195], v[154:157]
	v_mfma_f32_16x16x128_f8f6f4 v[138:141], v[10:17], v[196:203], v[138:141]
	v_mfma_f32_16x16x128_f8f6f4 v[142:145], v[2:9], v[196:203], v[142:145]
	v_mfma_f32_16x16x128_f8f6f4 v[110:113], v[2:9], v[212:219], v[110:113]
	v_mfma_f32_16x16x128_f8f6f4 v[106:109], v[10:17], v[212:219], v[106:109]
	v_mfma_f32_16x16x128_f8f6f4 v[102:105], v[18:25], v[212:219], v[102:105]
	v_mfma_f32_16x16x128_f8f6f4 v[98:101], v[26:33], v[212:219], v[98:101]
	v_mfma_f32_16x16x128_f8f6f4 v[146:149], v[26:33], v[188:195], v[146:149]
	v_mfma_f32_16x16x128_f8f6f4 v[150:153], v[18:25], v[188:195], v[150:153]
	v_mfma_f32_16x16x128_f8f6f4 v[134:137], v[18:25], v[196:203], v[134:137]
	v_mfma_f32_16x16x128_f8f6f4 v[130:133], v[26:33], v[196:203], v[130:133]
	v_mfma_f32_16x16x128_f8f6f4 v[114:117], v[26:33], v[204:211], v[114:117]
	v_mfma_f32_16x16x128_f8f6f4 v[118:121], v[18:25], v[204:211], v[118:121]
	s_setprio 0
	s_barrier
	s_add_i32 s24, s59, s3
	v_lshl_add_u64 v[174:175], v[174:175], 0, s[12:13]
	s_mov_b32 m0, s24
	ds_read_b128 v[188:191], v187 offset:49152
	ds_read_b128 v[192:195], v187 offset:50176
	ds_read_b128 v[196:199], v187 offset:51200
	ds_read_b128 v[200:203], v187 offset:52224
	ds_read_b128 v[204:207], v187 offset:53248
	ds_read_b128 v[208:211], v187 offset:54272
	ds_read_b128 v[212:215], v187 offset:55296
	ds_read_b128 v[216:219], v187 offset:56320
	global_load_lds_dwordx4 v[174:175], off
	s_add_i32 m0, s24, 0x2000
	s_add_u32 s24, s28, 0x158080
	v_lshl_add_u64 v[174:175], v[176:177], 0, s[12:13]
	s_addc_u32 s25, s29, 0
	s_add_i32 s28, s60, s3
	global_load_lds_dwordx4 v[174:175], off
	s_mov_b32 m0, s28
	s_nop 0
	global_load_lds_dwordx4 v164, s[24:25]
	s_add_i32 m0, s28, 0x2000
	s_nop 0
	global_load_lds_dwordx4 v162, s[24:25]
	v_lshl_add_u64 v[174:175], v[178:179], 0, s[12:13]
	s_mov_b32 m0, s38
	s_nop 0
	global_load_lds_dwordx4 v[174:175], off
	v_lshl_add_u64 v[174:175], v[180:181], 0, s[12:13]
	s_mov_b32 m0, s39
	s_nop 0
	global_load_lds_dwordx4 v[174:175], off
	s_waitcnt vmcnt(8)
	s_waitcnt lgkmcnt(0)
	s_barrier
	s_setprio 1
	v_mfma_f32_16x16x128_f8f6f4 v[62:65], v[2:9], v[204:211], v[62:65]
	v_mfma_f32_16x16x128_f8f6f4 v[58:61], v[10:17], v[204:211], v[58:61]
	v_mfma_f32_16x16x128_f8f6f4 v[90:93], v[10:17], v[188:195], v[90:93]
	v_mfma_f32_16x16x128_f8f6f4 v[94:97], v[2:9], v[188:195], v[94:97]
	v_mfma_f32_16x16x128_f8f6f4 v[78:81], v[2:9], v[196:203], v[78:81]
	v_mfma_f32_16x16x128_f8f6f4 v[74:77], v[10:17], v[196:203], v[74:77]
	v_mfma_f32_16x16x128_f8f6f4 v[42:45], v[10:17], v[212:219], v[42:45]
	v_mfma_f32_16x16x128_f8f6f4 v[46:49], v[2:9], v[212:219], v[46:49]
	v_mfma_f32_16x16x128_f8f6f4 v[38:41], v[18:25], v[212:219], v[38:41]
	v_mfma_f32_16x16x128_f8f6f4 v[34:37], v[26:33], v[212:219], v[34:37]
	v_mfma_f32_16x16x128_f8f6f4 v[82:85], v[26:33], v[188:195], v[82:85]
	v_mfma_f32_16x16x128_f8f6f4 v[86:89], v[18:25], v[188:195], v[86:89]
	v_mfma_f32_16x16x128_f8f6f4 v[70:73], v[18:25], v[196:203], v[70:73]
	v_mfma_f32_16x16x128_f8f6f4 v[66:69], v[26:33], v[196:203], v[66:69]
	v_mfma_f32_16x16x128_f8f6f4 v[50:53], v[26:33], v[204:211], v[50:53]
	v_mfma_f32_16x16x128_f8f6f4 v[54:57], v[18:25], v[204:211], v[54:57]
	s_setprio 0
	s_barrier
	s_add_i32 s58, s58, 2
	s_add_u32 s26, s26, 0x100
	s_addc_u32 s27, s27, 0
	s_add_u32 s50, s50, 0x100
	s_addc_u32 s51, s51, 0
	s_cmpk_gt_u32 s58, 0x53
	s_cbranch_scc0 .LBB0_318
	s_and_b64 vcc, exec, s[14:15]
	s_cbranch_vccz .LBB0_321
	s_barrier

.LBB0_332:
	s_add_u32 s6, s61, s4
	s_addc_u32 s7, s62, s5
	s_add_u32 s6, s6, 0x32800100
	s_addc_u32 s7, s7, 0
	s_add_u32 s24, s63, s4
	s_addc_u32 s25, s68, s5
	s_add_i32 s64, 0, 0x10000
	s_cmpk_eq_i32 s4, 0x2a00
	s_cselect_b32 s13, s1, s7
	s_cselect_b32 s12, s0, s6
	s_cselect_b32 s7, s29, s25
	s_cselect_b32 s6, s28, s24
	s_add_i32 s65, 0, 0x14000
	v_add_u32_e32 v2, s64, v188
	v_add_u32_e32 v6, s65, v188
	ds_read_b128 v[26:29], v2
	ds_read_b128 v[30:33], v2 offset:1024
	ds_read_b128 v[18:21], v2 offset:2048
	ds_read_b128 v[22:25], v2 offset:3072
	ds_read_b128 v[10:13], v6
	ds_read_b128 v[14:17], v6 offset:1024
	ds_read_b128 v[2:5], v6 offset:2048
	ds_read_b128 v[6:9], v6 offset:3072
	v_lshl_add_u64 v[214:215], v[168:169], 0, s[4:5]
	s_add_i32 m0, s18, 0xc000
	ds_read_b128 v[172:175], v189
	ds_read_b128 v[176:179], v189 offset:1024
	ds_read_b128 v[190:193], v189 offset:2048
	ds_read_b128 v[194:197], v189 offset:3072
	ds_read_b128 v[198:201], v189 offset:4096
	ds_read_b128 v[202:205], v189 offset:5120
	ds_read_b128 v[206:209], v189 offset:6144
	ds_read_b128 v[210:213], v189 offset:7168
	global_load_lds_dwordx4 v[214:215], off
	v_lshl_add_u64 v[214:215], v[170:171], 0, s[4:5]
	s_add_i32 m0, s18, 0xe000
	s_nop 0
	global_load_lds_dwordx4 v[214:215], off
	s_waitcnt vmcnt(8)
	s_waitcnt lgkmcnt(0)
	s_barrier
	s_setprio 1
	v_mfma_f32_16x16x128_f8f6f4 v[70:73], v[26:33], v[172:179], v[70:73]
	v_mfma_f32_16x16x128_f8f6f4 v[66:69], v[18:25], v[172:179], v[66:69]
	v_mfma_f32_16x16x128_f8f6f4 v[74:77], v[18:25], v[190:197], v[74:77]
	v_mfma_f32_16x16x128_f8f6f4 v[78:81], v[26:33], v[190:197], v[78:81]
	v_mfma_f32_16x16x128_f8f6f4 v[86:89], v[26:33], v[198:205], v[86:89]
	v_mfma_f32_16x16x128_f8f6f4 v[82:85], v[18:25], v[198:205], v[82:85]
	v_mfma_f32_16x16x128_f8f6f4 v[90:93], v[18:25], v[206:213], v[90:93]
	v_mfma_f32_16x16x128_f8f6f4 v[94:97], v[26:33], v[206:213], v[94:97]
	v_mfma_f32_16x16x128_f8f6f4 v[134:137], v[10:17], v[206:213], v[134:137]
	v_mfma_f32_16x16x128_f8f6f4 v[130:133], v[2:9], v[206:213], v[130:133]
	v_mfma_f32_16x16x128_f8f6f4 v[154:157], v[2:9], v[172:179], v[154:157]
	v_mfma_f32_16x16x128_f8f6f4 v[158:161], v[10:17], v[172:179], v[158:161]
	v_mfma_f32_16x16x128_f8f6f4 v[150:153], v[10:17], v[190:197], v[150:153]
	v_mfma_f32_16x16x128_f8f6f4 v[146:149], v[2:9], v[190:197], v[146:149]
	v_mfma_f32_16x16x128_f8f6f4 v[138:141], v[2:9], v[198:205], v[138:141]
	v_mfma_f32_16x16x128_f8f6f4 v[142:145], v[10:17], v[198:205], v[142:145]
	s_setprio 0
	s_barrier
	s_add_i32 s24, s64, s17
	v_lshl_add_u64 v[172:173], s[6:7], 0, v[162:163]
	s_mov_b32 m0, s24
	ds_read_b128 v[190:193], v189 offset:16384
	ds_read_b128 v[194:197], v189 offset:17408
	ds_read_b128 v[198:201], v189 offset:18432
	ds_read_b128 v[202:205], v189 offset:19456
	ds_read_b128 v[206:209], v189 offset:20480
	ds_read_b128 v[210:213], v189 offset:21504
	ds_read_b128 v[214:217], v189 offset:22528
	ds_read_b128 v[218:221], v189 offset:23552
	global_load_lds_dwordx4 v[172:173], off
	s_add_i32 m0, s24, 0x2000
	s_add_u32 s24, s6, 0x158000
	v_lshl_add_u64 v[174:175], s[6:7], 0, v[166:167]
	s_addc_u32 s25, s7, 0
	s_add_i32 s64, s65, s17
	global_load_lds_dwordx4 v[174:175], off
	s_mov_b32 m0, s64
	v_lshl_add_u64 v[178:179], s[12:13], 0, v[166:167]
	global_load_lds_dwordx4 v162, s[24:25]
	s_add_i32 m0, s64, 0x2000
	s_nop 0
	global_load_lds_dwordx4 v166, s[24:25]
	v_lshl_add_u64 v[176:177], s[12:13], 0, v[162:163]
	s_mov_b32 m0, s18
	s_nop 0
	global_load_lds_dwordx4 v[176:177], off
	s_mov_b32 m0, s19
	s_nop 0
	global_load_lds_dwordx4 v[178:179], off
	s_waitcnt vmcnt(8)
	s_waitcnt lgkmcnt(0)
	s_barrier
	s_setprio 1
	v_mfma_f32_16x16x128_f8f6f4 v[110:113], v[26:33], v[198:205], v[110:113]
	v_mfma_f32_16x16x128_f8f6f4 v[106:109], v[18:25], v[198:205], v[106:109]
	v_mfma_f32_16x16x128_f8f6f4 v[98:101], v[18:25], v[190:197], v[98:101]
	v_mfma_f32_16x16x128_f8f6f4 v[102:105], v[26:33], v[190:197], v[102:105]
	v_mfma_f32_16x16x128_f8f6f4 v[118:121], v[26:33], v[206:213], v[118:121]
	v_mfma_f32_16x16x128_f8f6f4 v[114:117], v[18:25], v[206:213], v[114:117]
	v_mfma_f32_16x16x128_f8f6f4 v[122:125], v[18:25], v[214:221], v[122:125]
	v_mfma_f32_16x16x128_f8f6f4 v[126:129], v[26:33], v[214:221], v[126:129]
	v_mfma_f32_16x16x128_f8f6f4 v[62:65], v[10:17], v[214:221], v[62:65]
	v_mfma_f32_16x16x128_f8f6f4 v[58:61], v[2:9], v[214:221], v[58:61]
	v_mfma_f32_16x16x128_f8f6f4 v[34:37], v[2:9], v[190:197], v[34:37]
	v_mfma_f32_16x16x128_f8f6f4 v[38:41], v[10:17], v[190:197], v[38:41]
	v_mfma_f32_16x16x128_f8f6f4 v[46:49], v[10:17], v[198:205], v[46:49]
	v_mfma_f32_16x16x128_f8f6f4 v[42:45], v[2:9], v[198:205], v[42:45]
	v_mfma_f32_16x16x128_f8f6f4 v[50:53], v[2:9], v[206:213], v[50:53]
	v_mfma_f32_16x16x128_f8f6f4 v[54:57], v[10:17], v[206:213], v[54:57]
	s_setprio 0
	s_barrier
	s_add_i32 s24, 0, 0x18000
	s_add_i32 s25, 0, 0x1c000
	v_add_u32_e32 v14, s24, v188
	v_add_u32_e32 v30, s25, v188
	ds_read_b128 v[2:5], v14
	ds_read_b128 v[6:9], v14 offset:1024
	ds_read_b128 v[10:13], v14 offset:2048
	ds_read_b128 v[14:17], v14 offset:3072
	ds_read_b128 v[18:21], v30
	ds_read_b128 v[22:25], v30 offset:1024
	ds_read_b128 v[26:29], v30 offset:2048
	ds_read_b128 v[30:33], v30 offset:3072
	s_add_u32 s12, s12, 0x158000
	s_addc_u32 s13, s13, 0
	s_mov_b32 m0, s93
	ds_read_b128 v[190:193], v189 offset:32768
	ds_read_b128 v[194:197], v189 offset:33792
	ds_read_b128 v[198:201], v189 offset:34816
	ds_read_b128 v[202:205], v189 offset:35840
	ds_read_b128 v[206:209], v189 offset:36864
	ds_read_b128 v[210:213], v189 offset:37888
	ds_read_b128 v[214:217], v189 offset:38912
	ds_read_b128 v[218:221], v189 offset:39936
	global_load_lds_dwordx4 v162, s[12:13]
	s_mov_b32 m0, s94
	s_nop 0
	global_load_lds_dwordx4 v166, s[12:13]
	s_waitcnt vmcnt(8)
	s_waitcnt lgkmcnt(0)
	s_barrier
	s_setprio 1
	v_mfma_f32_16x16x128_f8f6f4 v[82:85], v[10:17], v[206:213], v[82:85]
	v_mfma_f32_16x16x128_f8f6f4 v[86:89], v[2:9], v[206:213], v[86:89]
	v_mfma_f32_16x16x128_f8f6f4 v[70:73], v[2:9], v[190:197], v[70:73]
	v_mfma_f32_16x16x128_f8f6f4 v[66:69], v[10:17], v[190:197], v[66:69]
	v_mfma_f32_16x16x128_f8f6f4 v[74:77], v[10:17], v[198:205], v[74:77]
	v_mfma_f32_16x16x128_f8f6f4 v[78:81], v[2:9], v[198:205], v[78:81]
	v_mfma_f32_16x16x128_f8f6f4 v[94:97], v[2:9], v[214:221], v[94:97]
	v_mfma_f32_16x16x128_f8f6f4 v[90:93], v[10:17], v[214:221], v[90:93]
	v_mfma_f32_16x16x128_f8f6f4 v[134:137], v[18:25], v[214:221], v[134:137]
	v_mfma_f32_16x16x128_f8f6f4 v[130:133], v[26:33], v[214:221], v[130:133]
	v_mfma_f32_16x16x128_f8f6f4 v[154:157], v[26:33], v[190:197], v[154:157]
	v_mfma_f32_16x16x128_f8f6f4 v[158:161], v[18:25], v[190:197], v[158:161]
	v_mfma_f32_16x16x128_f8f6f4 v[150:153], v[18:25], v[198:205], v[150:153]
	v_mfma_f32_16x16x128_f8f6f4 v[146:149], v[26:33], v[198:205], v[146:149]
	v_mfma_f32_16x16x128_f8f6f4 v[138:141], v[26:33], v[206:213], v[138:141]
	v_mfma_f32_16x16x128_f8f6f4 v[142:145], v[18:25], v[206:213], v[142:145]
	s_setprio 0
	s_barrier
	s_add_i32 s12, s24, s17
	v_lshl_add_u64 v[172:173], v[172:173], 0, s[76:77]
	s_mov_b32 m0, s12
	ds_read_b128 v[190:193], v189 offset:49152
	ds_read_b128 v[194:197], v189 offset:50176
	ds_read_b128 v[198:201], v189 offset:51200
	ds_read_b128 v[202:205], v189 offset:52224
	ds_read_b128 v[206:209], v189 offset:53248
	ds_read_b128 v[210:213], v189 offset:54272
	ds_read_b128 v[214:217], v189 offset:55296
	ds_read_b128 v[218:221], v189 offset:56320
	global_load_lds_dwordx4 v[172:173], off
	s_add_i32 m0, s12, 0x2000
	s_add_u32 s6, s6, 0x158080
	v_lshl_add_u64 v[172:173], v[174:175], 0, s[76:77]
	s_addc_u32 s7, s7, 0
	s_add_i32 s12, s25, s17
	global_load_lds_dwordx4 v[172:173], off
	s_mov_b32 m0, s12
	s_nop 0
	global_load_lds_dwordx4 v162, s[6:7]
	s_add_i32 m0, s12, 0x2000
	s_nop 0
	global_load_lds_dwordx4 v166, s[6:7]
	v_lshl_add_u64 v[172:173], v[176:177], 0, s[76:77]
	s_mov_b32 m0, s95
	s_nop 0
	global_load_lds_dwordx4 v[172:173], off
	v_lshl_add_u64 v[172:173], v[178:179], 0, s[76:77]
	s_mov_b32 m0, vcc_lo
	s_nop 0
	global_load_lds_dwordx4 v[172:173], off
	s_waitcnt vmcnt(8)
	s_waitcnt lgkmcnt(0)
	s_barrier
	s_setprio 1
	v_mfma_f32_16x16x128_f8f6f4 v[118:121], v[2:9], v[206:213], v[118:121]
	v_mfma_f32_16x16x128_f8f6f4 v[114:117], v[10:17], v[206:213], v[114:117]
	v_mfma_f32_16x16x128_f8f6f4 v[98:101], v[10:17], v[190:197], v[98:101]
	v_mfma_f32_16x16x128_f8f6f4 v[102:105], v[2:9], v[190:197], v[102:105]
	v_mfma_f32_16x16x128_f8f6f4 v[110:113], v[2:9], v[198:205], v[110:113]
	v_mfma_f32_16x16x128_f8f6f4 v[106:109], v[10:17], v[198:205], v[106:109]
	v_mfma_f32_16x16x128_f8f6f4 v[122:125], v[10:17], v[214:221], v[122:125]
	v_mfma_f32_16x16x128_f8f6f4 v[126:129], v[2:9], v[214:221], v[126:129]
	v_mfma_f32_16x16x128_f8f6f4 v[62:65], v[18:25], v[214:221], v[62:65]
	v_mfma_f32_16x16x128_f8f6f4 v[58:61], v[26:33], v[214:221], v[58:61]
	v_mfma_f32_16x16x128_f8f6f4 v[34:37], v[26:33], v[190:197], v[34:37]
	v_mfma_f32_16x16x128_f8f6f4 v[38:41], v[18:25], v[190:197], v[38:41]
	v_mfma_f32_16x16x128_f8f6f4 v[46:49], v[18:25], v[198:205], v[46:49]
	v_mfma_f32_16x16x128_f8f6f4 v[42:45], v[26:33], v[198:205], v[42:45]
	v_mfma_f32_16x16x128_f8f6f4 v[50:53], v[26:33], v[206:213], v[50:53]
	v_mfma_f32_16x16x128_f8f6f4 v[54:57], v[18:25], v[206:213], v[54:57]
	s_setprio 0
	s_barrier
	s_add_i32 vcc_hi, vcc_hi, 2
	s_add_u32 s4, s4, 0x100
	s_addc_u32 s5, s5, 0
	s_cmpk_lt_u32 vcc_hi, 0x54
	s_cbranch_scc1 .LBB0_332
	s_waitcnt vmcnt(0)
	s_mov_b64 s[12:13], s[54:55]
	s_cmpk_gt_u32 s89, 0xff
	s_cbranch_scc1 .LBB0_335
	s_barrier

.LBB0_1291:
	ds_read_b128 v[26:29], v184
	ds_read_b128 v[30:33], v184 offset:1024
	ds_read_b128 v[18:21], v184 offset:2048
	ds_read_b128 v[22:25], v184 offset:3072
	ds_read_b128 v[10:13], v185
	ds_read_b128 v[14:17], v185 offset:1024
	ds_read_b128 v[2:5], v185 offset:2048
	ds_read_b128 v[6:9], v185 offset:3072
	s_add_u32 s20, s14, s16
	s_addc_u32 s21, s15, s17
	s_add_u32 s20, s20, 0x2a800100
	s_addc_u32 s21, s21, 0
	s_add_u32 s48, s31, s16
	s_addc_u32 s49, s34, s17
	s_cmpk_eq_i32 s16, 0x700
	s_cselect_b32 s23, s9, s21
	s_cselect_b32 s22, s8, s20
	s_cselect_b32 s21, s5, s49
	s_cselect_b32 s20, s4, s48
	s_mov_b32 m0, s36
	v_lshl_add_u64 v[214:215], v[170:171], 0, s[16:17]
	ds_read_b128 v[174:177], v186
	ds_read_b128 v[178:181], v186 offset:1024
	ds_read_b128 v[190:193], v186 offset:2048
	ds_read_b128 v[194:197], v186 offset:3072
	ds_read_b128 v[198:201], v186 offset:4096
	ds_read_b128 v[202:205], v186 offset:5120
	ds_read_b128 v[206:209], v186 offset:6144
	ds_read_b128 v[210:213], v186 offset:7168
	global_load_lds_dwordx4 v[214:215], off
	v_lshl_add_u64 v[214:215], v[172:173], 0, s[16:17]
	s_mov_b32 m0, s37
	s_nop 0
	global_load_lds_dwordx4 v[214:215], off
	s_waitcnt vmcnt(8)
	s_waitcnt lgkmcnt(0)
	s_barrier
	s_setprio 1
	v_mfma_f32_16x16x128_f8f6f4 v[158:161], v[26:33], v[174:181], v[158:161]
	v_mfma_f32_16x16x128_f8f6f4 v[154:157], v[18:25], v[174:181], v[154:157]
	v_mfma_f32_16x16x128_f8f6f4 v[138:141], v[18:25], v[190:197], v[138:141]
	v_mfma_f32_16x16x128_f8f6f4 v[146:149], v[26:33], v[190:197], v[146:149]
	v_mfma_f32_16x16x128_f8f6f4 v[130:133], v[26:33], v[198:205], v[130:133]
	v_mfma_f32_16x16x128_f8f6f4 v[122:125], v[18:25], v[198:205], v[122:125]
	v_mfma_f32_16x16x128_f8f6f4 v[106:109], v[18:25], v[206:213], v[106:109]
	v_mfma_f32_16x16x128_f8f6f4 v[114:117], v[26:33], v[206:213], v[114:117]
	v_mfma_f32_16x16x128_f8f6f4 v[102:105], v[10:17], v[206:213], v[102:105]
	v_mfma_f32_16x16x128_f8f6f4 v[98:101], v[2:9], v[206:213], v[98:101]
	v_mfma_f32_16x16x128_f8f6f4 v[142:145], v[2:9], v[174:181], v[142:145]
	v_mfma_f32_16x16x128_f8f6f4 v[150:153], v[10:17], v[174:181], v[150:153]
	v_mfma_f32_16x16x128_f8f6f4 v[134:137], v[10:17], v[190:197], v[134:137]
	v_mfma_f32_16x16x128_f8f6f4 v[126:129], v[2:9], v[190:197], v[126:129]
	v_mfma_f32_16x16x128_f8f6f4 v[110:113], v[2:9], v[198:205], v[110:113]
	v_mfma_f32_16x16x128_f8f6f4 v[118:121], v[10:17], v[198:205], v[118:121]
	s_setprio 0
	s_barrier
	s_mov_b32 m0, s38
	v_lshl_add_u64 v[174:175], s[20:21], 0, v[164:165]
	s_add_u32 s48, s20, 0x80000
	ds_read_b128 v[190:193], v186 offset:16384
	ds_read_b128 v[194:197], v186 offset:17408
	ds_read_b128 v[198:201], v186 offset:18432
	ds_read_b128 v[202:205], v186 offset:19456
	ds_read_b128 v[206:209], v186 offset:20480
	ds_read_b128 v[210:213], v186 offset:21504
	ds_read_b128 v[214:217], v186 offset:22528
	ds_read_b128 v[218:221], v186 offset:23552
	global_load_lds_dwordx4 v[174:175], off
	v_lshl_add_u64 v[176:177], s[20:21], 0, v[168:169]
	s_mov_b32 m0, s39
	s_addc_u32 s49, s21, 0
	global_load_lds_dwordx4 v[176:177], off
	s_mov_b32 m0, s40
	v_lshl_add_u64 v[180:181], s[22:23], 0, v[166:167]
	global_load_lds_dwordx4 v164, s[48:49]
	s_mov_b32 m0, s41
	s_nop 0
	global_load_lds_dwordx4 v168, s[48:49]
	v_lshl_add_u64 v[178:179], s[22:23], 0, v[162:163]
	s_mov_b32 m0, s24
	s_nop 0
	global_load_lds_dwordx4 v[178:179], off
	s_mov_b32 m0, s25
	s_nop 0
	global_load_lds_dwordx4 v[180:181], off
	s_waitcnt vmcnt(8)
	s_waitcnt lgkmcnt(0)
	s_barrier
	s_setprio 1
	v_mfma_f32_16x16x128_f8f6f4 v[82:85], v[26:33], v[198:205], v[82:85]
	v_mfma_f32_16x16x128_f8f6f4 v[74:77], v[18:25], v[198:205], v[74:77]
	v_mfma_f32_16x16x128_f8f6f4 v[90:93], v[18:25], v[190:197], v[90:93]
	v_mfma_f32_16x16x128_f8f6f4 v[94:97], v[26:33], v[190:197], v[94:97]
	v_mfma_f32_16x16x128_f8f6f4 v[66:69], v[26:33], v[206:213], v[66:69]
	v_mfma_f32_16x16x128_f8f6f4 v[58:61], v[18:25], v[206:213], v[58:61]
	v_mfma_f32_16x16x128_f8f6f4 v[42:45], v[18:25], v[214:221], v[42:45]
	v_mfma_f32_16x16x128_f8f6f4 v[50:53], v[26:33], v[214:221], v[50:53]
	v_mfma_f32_16x16x128_f8f6f4 v[38:41], v[10:17], v[214:221], v[38:41]
	v_mfma_f32_16x16x128_f8f6f4 v[34:37], v[2:9], v[214:221], v[34:37]
	v_mfma_f32_16x16x128_f8f6f4 v[78:81], v[2:9], v[190:197], v[78:81]
	v_mfma_f32_16x16x128_f8f6f4 v[86:89], v[10:17], v[190:197], v[86:89]
	v_mfma_f32_16x16x128_f8f6f4 v[70:73], v[10:17], v[198:205], v[70:73]
	v_mfma_f32_16x16x128_f8f6f4 v[62:65], v[2:9], v[198:205], v[62:65]
	v_mfma_f32_16x16x128_f8f6f4 v[46:49], v[2:9], v[206:213], v[46:49]
	v_mfma_f32_16x16x128_f8f6f4 v[54:57], v[10:17], v[206:213], v[54:57]
	s_setprio 0
	s_barrier
	ds_read_b128 v[2:5], v187
	ds_read_b128 v[6:9], v187 offset:1024
	ds_read_b128 v[10:13], v187 offset:2048
	ds_read_b128 v[14:17], v187 offset:3072
	ds_read_b128 v[18:21], v188
	ds_read_b128 v[22:25], v188 offset:1024
	ds_read_b128 v[26:29], v188 offset:2048
	ds_read_b128 v[30:33], v188 offset:3072
	s_add_u32 s22, s22, 0x80000
	s_addc_u32 s23, s23, 0
	s_mov_b32 m0, s26
	ds_read_b128 v[190:193], v186 offset:32768
	ds_read_b128 v[194:197], v186 offset:33792
	ds_read_b128 v[198:201], v186 offset:34816
	ds_read_b128 v[202:205], v186 offset:35840
	ds_read_b128 v[206:209], v186 offset:36864
	ds_read_b128 v[210:213], v186 offset:37888
	ds_read_b128 v[214:217], v186 offset:38912
	ds_read_b128 v[218:221], v186 offset:39936
	global_load_lds_dwordx4 v162, s[22:23]
	s_mov_b32 m0, s27
	s_nop 0
	global_load_lds_dwordx4 v166, s[22:23]
	s_waitcnt vmcnt(8)
	s_waitcnt lgkmcnt(0)
	s_barrier
	s_setprio 1
	v_mfma_f32_16x16x128_f8f6f4 v[122:125], v[10:17], v[206:213], v[122:125]
	v_mfma_f32_16x16x128_f8f6f4 v[130:133], v[2:9], v[206:213], v[130:133]
	v_mfma_f32_16x16x128_f8f6f4 v[158:161], v[2:9], v[190:197], v[158:161]
	v_mfma_f32_16x16x128_f8f6f4 v[154:157], v[10:17], v[190:197], v[154:157]
	v_mfma_f32_16x16x128_f8f6f4 v[138:141], v[10:17], v[198:205], v[138:141]
	v_mfma_f32_16x16x128_f8f6f4 v[146:149], v[2:9], v[198:205], v[146:149]
	v_mfma_f32_16x16x128_f8f6f4 v[114:117], v[2:9], v[214:221], v[114:117]
	v_mfma_f32_16x16x128_f8f6f4 v[106:109], v[10:17], v[214:221], v[106:109]
	v_mfma_f32_16x16x128_f8f6f4 v[102:105], v[18:25], v[214:221], v[102:105]
	v_mfma_f32_16x16x128_f8f6f4 v[98:101], v[26:33], v[214:221], v[98:101]
	v_mfma_f32_16x16x128_f8f6f4 v[142:145], v[26:33], v[190:197], v[142:145]
	v_mfma_f32_16x16x128_f8f6f4 v[150:153], v[18:25], v[190:197], v[150:153]
	v_mfma_f32_16x16x128_f8f6f4 v[134:137], v[18:25], v[198:205], v[134:137]
	v_mfma_f32_16x16x128_f8f6f4 v[126:129], v[26:33], v[198:205], v[126:129]
	v_mfma_f32_16x16x128_f8f6f4 v[110:113], v[26:33], v[206:213], v[110:113]
	v_mfma_f32_16x16x128_f8f6f4 v[118:121], v[18:25], v[206:213], v[118:121]
	s_setprio 0
	s_barrier
	s_mov_b32 m0, s42
	v_lshl_add_u64 v[174:175], v[174:175], 0, s[12:13]
	s_add_u32 s20, s20, 0x80080
	ds_read_b128 v[190:193], v186 offset:49152
	ds_read_b128 v[194:197], v186 offset:50176
	ds_read_b128 v[198:201], v186 offset:51200
	ds_read_b128 v[202:205], v186 offset:52224
	ds_read_b128 v[206:209], v186 offset:53248
	ds_read_b128 v[210:213], v186 offset:54272
	ds_read_b128 v[214:217], v186 offset:55296
	ds_read_b128 v[218:221], v186 offset:56320
	global_load_lds_dwordx4 v[174:175], off
	v_lshl_add_u64 v[174:175], v[176:177], 0, s[12:13]
	s_mov_b32 m0, s43
	s_addc_u32 s21, s21, 0
	global_load_lds_dwordx4 v[174:175], off
	s_mov_b32 m0, s44
	s_nop 0
	global_load_lds_dwordx4 v164, s[20:21]
	s_mov_b32 m0, s45
	s_nop 0
	global_load_lds_dwordx4 v168, s[20:21]
	v_lshl_add_u64 v[174:175], v[178:179], 0, s[12:13]
	s_mov_b32 m0, s29
	s_nop 0
	global_load_lds_dwordx4 v[174:175], off
	v_lshl_add_u64 v[174:175], v[180:181], 0, s[12:13]
	s_mov_b32 m0, s30
	s_nop 0
	global_load_lds_dwordx4 v[174:175], off
	s_waitcnt vmcnt(8)
	s_waitcnt lgkmcnt(0)
	s_barrier
	s_setprio 1
	v_mfma_f32_16x16x128_f8f6f4 v[66:69], v[2:9], v[206:213], v[66:69]
	v_mfma_f32_16x16x128_f8f6f4 v[58:61], v[10:17], v[206:213], v[58:61]
	v_mfma_f32_16x16x128_f8f6f4 v[90:93], v[10:17], v[190:197], v[90:93]
	v_mfma_f32_16x16x128_f8f6f4 v[94:97], v[2:9], v[190:197], v[94:97]
	v_mfma_f32_16x16x128_f8f6f4 v[82:85], v[2:9], v[198:205], v[82:85]
	v_mfma_f32_16x16x128_f8f6f4 v[74:77], v[10:17], v[198:205], v[74:77]
	v_mfma_f32_16x16x128_f8f6f4 v[42:45], v[10:17], v[214:221], v[42:45]
	v_mfma_f32_16x16x128_f8f6f4 v[50:53], v[2:9], v[214:221], v[50:53]
	v_mfma_f32_16x16x128_f8f6f4 v[38:41], v[18:25], v[214:221], v[38:41]
	v_mfma_f32_16x16x128_f8f6f4 v[34:37], v[26:33], v[214:221], v[34:37]
	v_mfma_f32_16x16x128_f8f6f4 v[78:81], v[26:33], v[190:197], v[78:81]
	v_mfma_f32_16x16x128_f8f6f4 v[86:89], v[18:25], v[190:197], v[86:89]
	v_mfma_f32_16x16x128_f8f6f4 v[70:73], v[18:25], v[198:205], v[70:73]
	v_mfma_f32_16x16x128_f8f6f4 v[62:65], v[26:33], v[198:205], v[62:65]
	v_mfma_f32_16x16x128_f8f6f4 v[46:49], v[26:33], v[206:213], v[46:49]
	v_mfma_f32_16x16x128_f8f6f4 v[54:57], v[18:25], v[206:213], v[54:57]
	s_setprio 0
	s_barrier
	s_add_i32 s35, s35, 2
	s_add_u32 s16, s16, 0x100
	s_addc_u32 s17, s17, 0
	s_cmp_gt_u32 s35, 13
	s_cbranch_scc0 .LBB0_1291
	s_cmpk_lt_u32 s19, 0x100
	s_cbranch_scc0 .LBB0_1294
	s_barrier

.LBB0_1309:
	ds_read_b128 v[26:29], v189
	ds_read_b128 v[30:33], v189 offset:1024
	ds_read_b128 v[18:21], v189 offset:2048
	ds_read_b128 v[22:25], v189 offset:3072
	ds_read_b128 v[10:13], v190
	ds_read_b128 v[14:17], v190 offset:1024
	ds_read_b128 v[2:5], v190 offset:2048
	ds_read_b128 v[6:9], v190 offset:3072
	s_add_u32 s40, s38, 0xfff80080
	s_addc_u32 s41, s39, -1
	s_cmp_eq_u32 s72, 28
	s_cselect_b32 s43, s18, s41
	s_cselect_b32 s42, s19, s40
	s_cselect_b32 s41, s27, s71
	s_cselect_b32 s40, s29, s70
	s_add_i32 m0, s37, 0xc000
	ds_read_b128 v[178:181], v191
	ds_read_b128 v[182:185], v191 offset:1024
	ds_read_b128 v[192:195], v191 offset:2048
	ds_read_b128 v[196:199], v191 offset:3072
	ds_read_b128 v[200:203], v191 offset:4096
	ds_read_b128 v[204:207], v191 offset:5120
	ds_read_b128 v[208:211], v191 offset:6144
	ds_read_b128 v[212:215], v191 offset:7168
	global_load_lds_dwordx4 v170, s[38:39]
	v_lshl_add_u64 v[216:217], s[38:39], 0, v[172:173]
	s_add_i32 m0, s37, 0xe000
	s_nop 0
	global_load_lds_dwordx4 v[216:217], off
	s_waitcnt vmcnt(8)
	s_waitcnt lgkmcnt(0)
	s_barrier
	s_setprio 1
	v_mfma_f32_16x16x128_f8f6f4 v[158:161], v[26:33], v[178:185], v[158:161]
	v_mfma_f32_16x16x128_f8f6f4 v[154:157], v[18:25], v[178:185], v[154:157]
	v_mfma_f32_16x16x128_f8f6f4 v[138:141], v[18:25], v[192:199], v[138:141]
	v_mfma_f32_16x16x128_f8f6f4 v[146:149], v[26:33], v[192:199], v[146:149]
	v_mfma_f32_16x16x128_f8f6f4 v[130:133], v[26:33], v[200:207], v[130:133]
	v_mfma_f32_16x16x128_f8f6f4 v[122:125], v[18:25], v[200:207], v[122:125]
	v_mfma_f32_16x16x128_f8f6f4 v[106:109], v[18:25], v[208:215], v[106:109]
	v_mfma_f32_16x16x128_f8f6f4 v[114:117], v[26:33], v[208:215], v[114:117]
	v_mfma_f32_16x16x128_f8f6f4 v[102:105], v[10:17], v[208:215], v[102:105]
	v_mfma_f32_16x16x128_f8f6f4 v[98:101], v[2:9], v[208:215], v[98:101]
	v_mfma_f32_16x16x128_f8f6f4 v[142:145], v[2:9], v[178:185], v[142:145]
	v_mfma_f32_16x16x128_f8f6f4 v[150:153], v[10:17], v[178:185], v[150:153]
	v_mfma_f32_16x16x128_f8f6f4 v[134:137], v[10:17], v[192:199], v[134:137]
	v_mfma_f32_16x16x128_f8f6f4 v[126:129], v[2:9], v[192:199], v[126:129]
	v_mfma_f32_16x16x128_f8f6f4 v[110:113], v[2:9], v[200:207], v[110:113]
	v_mfma_f32_16x16x128_f8f6f4 v[118:121], v[10:17], v[200:207], v[118:121]
	s_setprio 0
	s_barrier
	s_add_i32 s64, s59, s3
	v_lshl_add_u64 v[178:179], s[40:41], 0, v[166:167]
	s_mov_b32 m0, s64
	ds_read_b128 v[192:195], v191 offset:16384
	ds_read_b128 v[196:199], v191 offset:17408
	ds_read_b128 v[200:203], v191 offset:18432
	ds_read_b128 v[204:207], v191 offset:19456
	ds_read_b128 v[208:211], v191 offset:20480
	ds_read_b128 v[212:215], v191 offset:21504
	ds_read_b128 v[216:219], v191 offset:22528
	ds_read_b128 v[220:223], v191 offset:23552
	global_load_lds_dwordx4 v[178:179], off
	s_add_i32 m0, s64, 0x2000
	s_add_u32 s64, s40, 0x80000
	v_lshl_add_u64 v[180:181], s[40:41], 0, v[162:163]
	s_addc_u32 s65, s41, 0
	s_add_i32 s73, s62, s3
	global_load_lds_dwordx4 v[180:181], off
	s_mov_b32 m0, s73
	v_lshl_add_u64 v[184:185], s[42:43], 0, v[164:165]
	global_load_lds_dwordx4 v166, s[64:65]
	s_add_i32 m0, s73, 0x2000
	s_nop 0
	global_load_lds_dwordx4 v162, s[64:65]
	v_lshl_add_u64 v[182:183], s[42:43], 0, v[168:169]
	s_mov_b32 m0, s37
	s_nop 0
	global_load_lds_dwordx4 v[182:183], off
	s_mov_b32 m0, s44
	s_nop 0
	global_load_lds_dwordx4 v[184:185], off
	s_waitcnt vmcnt(8)
	s_waitcnt lgkmcnt(0)
	s_barrier
	s_setprio 1
	v_mfma_f32_16x16x128_f8f6f4 v[82:85], v[26:33], v[200:207], v[82:85]
	v_mfma_f32_16x16x128_f8f6f4 v[74:77], v[18:25], v[200:207], v[74:77]
	v_mfma_f32_16x16x128_f8f6f4 v[90:93], v[18:25], v[192:199], v[90:93]
	v_mfma_f32_16x16x128_f8f6f4 v[94:97], v[26:33], v[192:199], v[94:97]
	v_mfma_f32_16x16x128_f8f6f4 v[66:69], v[26:33], v[208:215], v[66:69]
	v_mfma_f32_16x16x128_f8f6f4 v[58:61], v[18:25], v[208:215], v[58:61]
	v_mfma_f32_16x16x128_f8f6f4 v[42:45], v[18:25], v[216:223], v[42:45]
	v_mfma_f32_16x16x128_f8f6f4 v[50:53], v[26:33], v[216:223], v[50:53]
	v_mfma_f32_16x16x128_f8f6f4 v[38:41], v[10:17], v[216:223], v[38:41]
	v_mfma_f32_16x16x128_f8f6f4 v[34:37], v[2:9], v[216:223], v[34:37]
	v_mfma_f32_16x16x128_f8f6f4 v[78:81], v[2:9], v[192:199], v[78:81]
	v_mfma_f32_16x16x128_f8f6f4 v[86:89], v[10:17], v[192:199], v[86:89]
	v_mfma_f32_16x16x128_f8f6f4 v[70:73], v[10:17], v[200:207], v[70:73]
	v_mfma_f32_16x16x128_f8f6f4 v[62:65], v[2:9], v[200:207], v[62:65]
	v_mfma_f32_16x16x128_f8f6f4 v[46:49], v[2:9], v[208:215], v[46:49]
	v_mfma_f32_16x16x128_f8f6f4 v[54:57], v[10:17], v[208:215], v[54:57]
	s_setprio 0
	s_barrier
	s_add_i32 s64, 0, 0x18000
	s_add_i32 s65, 0, 0x1c000
	v_add_u32_e32 v14, s64, v187
	v_add_u32_e32 v30, s65, v187
	ds_read_b128 v[2:5], v14
	ds_read_b128 v[6:9], v14 offset:1024
	ds_read_b128 v[10:13], v14 offset:2048
	ds_read_b128 v[14:17], v14 offset:3072
	ds_read_b128 v[18:21], v30
	ds_read_b128 v[22:25], v30 offset:1024
	ds_read_b128 v[26:29], v30 offset:2048
	ds_read_b128 v[30:33], v30 offset:3072
	s_add_u32 s42, s42, 0x80000
	s_addc_u32 s43, s43, 0
	s_mov_b32 m0, s45
	ds_read_b128 v[192:195], v191 offset:32768
	ds_read_b128 v[196:199], v191 offset:33792
	ds_read_b128 v[200:203], v191 offset:34816
	ds_read_b128 v[204:207], v191 offset:35840
	ds_read_b128 v[208:211], v191 offset:36864
	ds_read_b128 v[212:215], v191 offset:37888
	ds_read_b128 v[216:219], v191 offset:38912
	ds_read_b128 v[220:223], v191 offset:39936
	global_load_lds_dwordx4 v168, s[42:43]
	s_mov_b32 m0, s48
	s_nop 0
	global_load_lds_dwordx4 v164, s[42:43]
	s_waitcnt vmcnt(8)
	s_waitcnt lgkmcnt(0)
	s_barrier
	s_setprio 1
	v_mfma_f32_16x16x128_f8f6f4 v[122:125], v[10:17], v[208:215], v[122:125]
	v_mfma_f32_16x16x128_f8f6f4 v[130:133], v[2:9], v[208:215], v[130:133]
	v_mfma_f32_16x16x128_f8f6f4 v[158:161], v[2:9], v[192:199], v[158:161]
	v_mfma_f32_16x16x128_f8f6f4 v[154:157], v[10:17], v[192:199], v[154:157]
	v_mfma_f32_16x16x128_f8f6f4 v[138:141], v[10:17], v[200:207], v[138:141]
	v_mfma_f32_16x16x128_f8f6f4 v[146:149], v[2:9], v[200:207], v[146:149]
	v_mfma_f32_16x16x128_f8f6f4 v[114:117], v[2:9], v[216:223], v[114:117]
	v_mfma_f32_16x16x128_f8f6f4 v[106:109], v[10:17], v[216:223], v[106:109]
	v_mfma_f32_16x16x128_f8f6f4 v[102:105], v[18:25], v[216:223], v[102:105]
	v_mfma_f32_16x16x128_f8f6f4 v[98:101], v[26:33], v[216:223], v[98:101]
	v_mfma_f32_16x16x128_f8f6f4 v[142:145], v[26:33], v[192:199], v[142:145]
	v_mfma_f32_16x16x128_f8f6f4 v[150:153], v[18:25], v[192:199], v[150:153]
	v_mfma_f32_16x16x128_f8f6f4 v[134:137], v[18:25], v[200:207], v[134:137]
	v_mfma_f32_16x16x128_f8f6f4 v[126:129], v[26:33], v[200:207], v[126:129]
	v_mfma_f32_16x16x128_f8f6f4 v[110:113], v[26:33], v[208:215], v[110:113]
	v_mfma_f32_16x16x128_f8f6f4 v[118:121], v[18:25], v[208:215], v[118:121]
	s_setprio 0
	s_barrier
	s_add_i32 s42, s64, s3
	v_lshl_add_u64 v[178:179], v[178:179], 0, s[12:13]
	s_mov_b32 m0, s42
	ds_read_b128 v[192:195], v191 offset:49152
	ds_read_b128 v[196:199], v191 offset:50176
	ds_read_b128 v[200:203], v191 offset:51200
	ds_read_b128 v[204:207], v191 offset:52224
	ds_read_b128 v[208:211], v191 offset:53248
	ds_read_b128 v[212:215], v191 offset:54272
	ds_read_b128 v[216:219], v191 offset:55296
	ds_read_b128 v[220:223], v191 offset:56320
	global_load_lds_dwordx4 v[178:179], off
	s_add_i32 m0, s42, 0x2000
	s_add_u32 s40, s40, 0x80080
	v_lshl_add_u64 v[178:179], v[180:181], 0, s[12:13]
	s_addc_u32 s41, s41, 0
	s_add_i32 s42, s65, s3
	global_load_lds_dwordx4 v[178:179], off
	s_mov_b32 m0, s42
	s_nop 0
	global_load_lds_dwordx4 v166, s[40:41]
	s_add_i32 m0, s42, 0x2000
	s_nop 0
	global_load_lds_dwordx4 v162, s[40:41]
	v_lshl_add_u64 v[178:179], v[182:183], 0, s[12:13]
	s_mov_b32 m0, s51
	s_nop 0
	global_load_lds_dwordx4 v[178:179], off
	v_lshl_add_u64 v[178:179], v[184:185], 0, s[12:13]
	s_mov_b32 m0, s58
	s_nop 0
	global_load_lds_dwordx4 v[178:179], off
	s_waitcnt vmcnt(8)
	s_waitcnt lgkmcnt(0)
	s_barrier
	s_setprio 1
	v_mfma_f32_16x16x128_f8f6f4 v[66:69], v[2:9], v[208:215], v[66:69]
	v_mfma_f32_16x16x128_f8f6f4 v[58:61], v[10:17], v[208:215], v[58:61]
	v_mfma_f32_16x16x128_f8f6f4 v[90:93], v[10:17], v[192:199], v[90:93]
	v_mfma_f32_16x16x128_f8f6f4 v[94:97], v[2:9], v[192:199], v[94:97]
	v_mfma_f32_16x16x128_f8f6f4 v[82:85], v[2:9], v[200:207], v[82:85]
	v_mfma_f32_16x16x128_f8f6f4 v[74:77], v[10:17], v[200:207], v[74:77]
	v_mfma_f32_16x16x128_f8f6f4 v[42:45], v[10:17], v[216:223], v[42:45]
	v_mfma_f32_16x16x128_f8f6f4 v[50:53], v[2:9], v[216:223], v[50:53]
	v_mfma_f32_16x16x128_f8f6f4 v[38:41], v[18:25], v[216:223], v[38:41]
	v_mfma_f32_16x16x128_f8f6f4 v[34:37], v[26:33], v[216:223], v[34:37]
	v_mfma_f32_16x16x128_f8f6f4 v[78:81], v[26:33], v[192:199], v[78:81]
	v_mfma_f32_16x16x128_f8f6f4 v[86:89], v[18:25], v[192:199], v[86:89]
	v_mfma_f32_16x16x128_f8f6f4 v[70:73], v[18:25], v[200:207], v[70:73]
	v_mfma_f32_16x16x128_f8f6f4 v[62:65], v[26:33], v[200:207], v[62:65]
	v_mfma_f32_16x16x128_f8f6f4 v[46:49], v[26:33], v[208:215], v[46:49]
	v_mfma_f32_16x16x128_f8f6f4 v[54:57], v[18:25], v[208:215], v[54:57]
	s_setprio 0
	s_barrier
	s_add_i32 s72, s72, 2
	s_add_u32 s38, s38, 0x100
	s_addc_u32 s39, s39, 0
	s_add_u32 s70, s70, 0x100
	s_addc_u32 s71, s71, 0
	s_cmp_gt_u32 s72, 29
	s_cbranch_scc0 .LBB0_1309
	s_and_b64 vcc, exec, s[14:15]
	s_cbranch_vccz .LBB0_1312
	s_barrier

.LBB0_1558:
	s_add_u32 s39, s30, s38
	s_addc_u32 s44, s31, 0
	s_add_u32 s42, s39, 0x100
	s_addc_u32 s43, s44, 0
	s_and_b64 s[40:41], s[36:37], exec
	s_cselect_b32 s41, s18, s43
	s_cselect_b32 s40, s19, s42
	s_add_u32 s38, s28, s38
	s_addc_u32 s42, s29, 0
	s_add_u32 s38, s38, 0x100
	s_addc_u32 s42, s42, 0
	s_and_b64 s[36:37], s[36:37], exec
	s_cselect_b32 s43, s17, s42
	s_cselect_b32 s42, s21, s38
	s_add_u32 s76, s39, 0x10080
	ds_read_b128 v[26:29], v181
	ds_read_b128 v[30:33], v181 offset:1024
	ds_read_b128 v[18:21], v181 offset:2048
	ds_read_b128 v[22:25], v181 offset:3072
	ds_read_b128 v[10:13], v182
	ds_read_b128 v[14:17], v182 offset:1024
	ds_read_b128 v[2:5], v182 offset:2048
	ds_read_b128 v[6:9], v182 offset:3072
	s_addc_u32 s77, s44, 0
	s_add_i32 s75, s63, s15
	s_add_i32 m0, s27, 0xc000
	s_add_i32 s78, s27, 0xe000
	s_add_i32 s72, s75, 0x2000
	s_add_u32 s44, s42, 0x10000
	s_addc_u32 s45, s43, 0
	s_add_i32 s74, s64, s15
	s_add_i32 s73, s74, 0x2000
	s_add_i32 s71, 0, 0x18000
	s_add_i32 s70, 0, 0x1c000
	s_add_u32 s38, s40, 0x10000
	s_addc_u32 s39, s41, 0
	s_add_i32 s69, s71, s15
	s_add_i32 s67, s69, 0x2000
	s_add_u32 s36, s42, 0x10080
	s_addc_u32 s37, s43, 0
	s_add_i32 s68, s70, s15
	s_add_i32 s66, s68, 0x2000
	ds_read_b128 v[170:173], v183
	ds_read_b128 v[174:177], v183 offset:1024
	ds_read_b128 v[184:187], v183 offset:2048
	ds_read_b128 v[188:191], v183 offset:3072
	ds_read_b128 v[192:195], v183 offset:4096
	ds_read_b128 v[196:199], v183 offset:5120
	ds_read_b128 v[200:203], v183 offset:6144
	ds_read_b128 v[204:207], v183 offset:7168
	global_load_lds_dwordx4 v164, s[76:77]
	v_lshl_add_u64 v[208:209], s[76:77], 0, v[162:163]
	s_mov_b32 m0, s78
	s_nop 0
	global_load_lds_dwordx4 v[208:209], off
	s_waitcnt vmcnt(8)
	s_waitcnt lgkmcnt(0)
	s_barrier
	s_setprio 1
	v_mfma_f32_16x16x128_f8f6f4 v[158:161], v[26:33], v[170:177], v[158:161]
	v_mfma_f32_16x16x128_f8f6f4 v[154:157], v[18:25], v[170:177], v[154:157]
	v_mfma_f32_16x16x128_f8f6f4 v[138:141], v[18:25], v[184:191], v[138:141]
	v_mfma_f32_16x16x128_f8f6f4 v[142:145], v[26:33], v[184:191], v[142:145]
	v_mfma_f32_16x16x128_f8f6f4 v[126:129], v[26:33], v[192:199], v[126:129]
	v_mfma_f32_16x16x128_f8f6f4 v[122:125], v[18:25], v[192:199], v[122:125]
	v_mfma_f32_16x16x128_f8f6f4 v[106:109], v[18:25], v[200:207], v[106:109]
	v_mfma_f32_16x16x128_f8f6f4 v[110:113], v[26:33], v[200:207], v[110:113]
	v_mfma_f32_16x16x128_f8f6f4 v[102:105], v[10:17], v[200:207], v[102:105]
	v_mfma_f32_16x16x128_f8f6f4 v[98:101], v[2:9], v[200:207], v[98:101]
	v_mfma_f32_16x16x128_f8f6f4 v[146:149], v[2:9], v[170:177], v[146:149]
	v_mfma_f32_16x16x128_f8f6f4 v[150:153], v[10:17], v[170:177], v[150:153]
	v_mfma_f32_16x16x128_f8f6f4 v[134:137], v[10:17], v[184:191], v[134:137]
	v_mfma_f32_16x16x128_f8f6f4 v[130:133], v[2:9], v[184:191], v[130:133]
	v_mfma_f32_16x16x128_f8f6f4 v[114:117], v[2:9], v[192:199], v[114:117]
	v_mfma_f32_16x16x128_f8f6f4 v[118:121], v[10:17], v[192:199], v[118:121]
	s_setprio 0
	s_barrier
	s_mov_b32 m0, s75
	v_lshl_add_u64 v[170:171], s[42:43], 0, v[164:165]
	ds_read_b128 v[184:187], v183 offset:16384
	ds_read_b128 v[188:191], v183 offset:17408
	ds_read_b128 v[192:195], v183 offset:18432
	ds_read_b128 v[196:199], v183 offset:19456
	ds_read_b128 v[200:203], v183 offset:20480
	ds_read_b128 v[204:207], v183 offset:21504
	ds_read_b128 v[208:211], v183 offset:22528
	ds_read_b128 v[212:215], v183 offset:23552
	global_load_lds_dwordx4 v[170:171], off
	v_lshl_add_u64 v[172:173], s[42:43], 0, v[162:163]
	s_mov_b32 m0, s72
	global_load_lds_dwordx4 v[172:173], off
	s_mov_b32 m0, s74
	v_lshl_add_u64 v[176:177], s[40:41], 0, v[162:163]
	global_load_lds_dwordx4 v164, s[44:45]
	s_mov_b32 m0, s73
	s_nop 0
	global_load_lds_dwordx4 v162, s[44:45]
	v_lshl_add_u64 v[174:175], s[40:41], 0, v[164:165]
	s_mov_b32 m0, s27
	s_nop 0
	global_load_lds_dwordx4 v[174:175], off
	s_mov_b32 m0, s49
	s_nop 0
	global_load_lds_dwordx4 v[176:177], off
	s_waitcnt vmcnt(8)
	s_waitcnt lgkmcnt(0)
	s_barrier
	s_setprio 1
	v_mfma_f32_16x16x128_f8f6f4 v[78:81], v[26:33], v[192:199], v[78:81]
	v_mfma_f32_16x16x128_f8f6f4 v[74:77], v[18:25], v[192:199], v[74:77]
	v_mfma_f32_16x16x128_f8f6f4 v[90:93], v[18:25], v[184:191], v[90:93]
	v_mfma_f32_16x16x128_f8f6f4 v[94:97], v[26:33], v[184:191], v[94:97]
	v_mfma_f32_16x16x128_f8f6f4 v[62:65], v[26:33], v[200:207], v[62:65]
	v_mfma_f32_16x16x128_f8f6f4 v[58:61], v[18:25], v[200:207], v[58:61]
	v_mfma_f32_16x16x128_f8f6f4 v[42:45], v[18:25], v[208:215], v[42:45]
	v_mfma_f32_16x16x128_f8f6f4 v[54:57], v[26:33], v[208:215], v[54:57]
	v_mfma_f32_16x16x128_f8f6f4 v[38:41], v[10:17], v[208:215], v[38:41]
	v_mfma_f32_16x16x128_f8f6f4 v[34:37], v[2:9], v[208:215], v[34:37]
	v_mfma_f32_16x16x128_f8f6f4 v[82:85], v[2:9], v[184:191], v[82:85]
	v_mfma_f32_16x16x128_f8f6f4 v[86:89], v[10:17], v[184:191], v[86:89]
	v_mfma_f32_16x16x128_f8f6f4 v[70:73], v[10:17], v[192:199], v[70:73]
	v_mfma_f32_16x16x128_f8f6f4 v[66:69], v[2:9], v[192:199], v[66:69]
	v_mfma_f32_16x16x128_f8f6f4 v[46:49], v[2:9], v[200:207], v[46:49]
	v_mfma_f32_16x16x128_f8f6f4 v[50:53], v[10:17], v[200:207], v[50:53]
	s_setprio 0
	s_barrier
	v_add_u32_e32 v14, s71, v179
	v_add_u32_e32 v30, s70, v179
	ds_read_b128 v[2:5], v14
	ds_read_b128 v[6:9], v14 offset:1024
	ds_read_b128 v[10:13], v14 offset:2048
	ds_read_b128 v[14:17], v14 offset:3072
	ds_read_b128 v[18:21], v30
	ds_read_b128 v[22:25], v30 offset:1024
	ds_read_b128 v[26:29], v30 offset:2048
	ds_read_b128 v[30:33], v30 offset:3072
	s_mov_b32 m0, s50
	ds_read_b128 v[184:187], v183 offset:32768
	ds_read_b128 v[188:191], v183 offset:33792
	ds_read_b128 v[192:195], v183 offset:34816
	ds_read_b128 v[196:199], v183 offset:35840
	ds_read_b128 v[200:203], v183 offset:36864
	ds_read_b128 v[204:207], v183 offset:37888
	ds_read_b128 v[208:211], v183 offset:38912
	ds_read_b128 v[212:215], v183 offset:39936
	global_load_lds_dwordx4 v164, s[38:39]
	s_mov_b32 m0, s51
	s_nop 0
	global_load_lds_dwordx4 v162, s[38:39]
	s_waitcnt vmcnt(8)
	s_waitcnt lgkmcnt(0)
	s_barrier
	s_setprio 1
	v_mfma_f32_16x16x128_f8f6f4 v[122:125], v[10:17], v[200:207], v[122:125]
	v_mfma_f32_16x16x128_f8f6f4 v[126:129], v[2:9], v[200:207], v[126:129]
	v_mfma_f32_16x16x128_f8f6f4 v[158:161], v[2:9], v[184:191], v[158:161]
	v_mfma_f32_16x16x128_f8f6f4 v[154:157], v[10:17], v[184:191], v[154:157]
	v_mfma_f32_16x16x128_f8f6f4 v[138:141], v[10:17], v[192:199], v[138:141]
	v_mfma_f32_16x16x128_f8f6f4 v[142:145], v[2:9], v[192:199], v[142:145]
	v_mfma_f32_16x16x128_f8f6f4 v[110:113], v[2:9], v[208:215], v[110:113]
	v_mfma_f32_16x16x128_f8f6f4 v[106:109], v[10:17], v[208:215], v[106:109]
	v_mfma_f32_16x16x128_f8f6f4 v[102:105], v[18:25], v[208:215], v[102:105]
	v_mfma_f32_16x16x128_f8f6f4 v[98:101], v[26:33], v[208:215], v[98:101]
	v_mfma_f32_16x16x128_f8f6f4 v[146:149], v[26:33], v[184:191], v[146:149]
	v_mfma_f32_16x16x128_f8f6f4 v[150:153], v[18:25], v[184:191], v[150:153]
	v_mfma_f32_16x16x128_f8f6f4 v[134:137], v[18:25], v[192:199], v[134:137]
	v_mfma_f32_16x16x128_f8f6f4 v[130:133], v[26:33], v[192:199], v[130:133]
	v_mfma_f32_16x16x128_f8f6f4 v[114:117], v[26:33], v[200:207], v[114:117]
	v_mfma_f32_16x16x128_f8f6f4 v[118:121], v[18:25], v[200:207], v[118:121]
	s_setprio 0
	s_barrier
	s_mov_b32 m0, s69
	v_lshl_add_u64 v[170:171], v[170:171], 0, s[8:9]
	ds_read_b128 v[184:187], v183 offset:49152
	ds_read_b128 v[188:191], v183 offset:50176
	ds_read_b128 v[192:195], v183 offset:51200
	ds_read_b128 v[196:199], v183 offset:52224
	ds_read_b128 v[200:203], v183 offset:53248
	ds_read_b128 v[204:207], v183 offset:54272
	ds_read_b128 v[208:211], v183 offset:55296
	ds_read_b128 v[212:215], v183 offset:56320
	global_load_lds_dwordx4 v[170:171], off
	v_lshl_add_u64 v[170:171], v[172:173], 0, s[8:9]
	s_mov_b32 m0, s67
	s_nop 0
	global_load_lds_dwordx4 v[170:171], off
	s_mov_b32 m0, s68
	s_nop 0
	global_load_lds_dwordx4 v164, s[36:37]
	s_mov_b32 m0, s66
	s_nop 0
	global_load_lds_dwordx4 v162, s[36:37]
	v_lshl_add_u64 v[170:171], v[174:175], 0, s[8:9]
	s_mov_b32 m0, s61
	s_nop 0
	global_load_lds_dwordx4 v[170:171], off
	v_lshl_add_u64 v[170:171], v[176:177], 0, s[8:9]
	s_mov_b32 m0, s62
	s_nop 0
	global_load_lds_dwordx4 v[170:171], off
	s_waitcnt vmcnt(8)
	s_waitcnt lgkmcnt(0)
	s_barrier
	s_setprio 1
	v_mfma_f32_16x16x128_f8f6f4 v[62:65], v[2:9], v[200:207], v[62:65]
	v_mfma_f32_16x16x128_f8f6f4 v[58:61], v[10:17], v[200:207], v[58:61]
	v_mfma_f32_16x16x128_f8f6f4 v[90:93], v[10:17], v[184:191], v[90:93]
	v_mfma_f32_16x16x128_f8f6f4 v[94:97], v[2:9], v[184:191], v[94:97]
	v_mfma_f32_16x16x128_f8f6f4 v[78:81], v[2:9], v[192:199], v[78:81]
	v_mfma_f32_16x16x128_f8f6f4 v[74:77], v[10:17], v[192:199], v[74:77]
	v_mfma_f32_16x16x128_f8f6f4 v[42:45], v[10:17], v[208:215], v[42:45]
	v_mfma_f32_16x16x128_f8f6f4 v[54:57], v[2:9], v[208:215], v[54:57]
	v_mfma_f32_16x16x128_f8f6f4 v[38:41], v[18:25], v[208:215], v[38:41]
	v_mfma_f32_16x16x128_f8f6f4 v[34:37], v[26:33], v[208:215], v[34:37]
	v_mfma_f32_16x16x128_f8f6f4 v[82:85], v[26:33], v[184:191], v[82:85]
	v_mfma_f32_16x16x128_f8f6f4 v[86:89], v[18:25], v[184:191], v[86:89]
	v_mfma_f32_16x16x128_f8f6f4 v[70:73], v[18:25], v[192:199], v[70:73]
	v_mfma_f32_16x16x128_f8f6f4 v[66:69], v[26:33], v[192:199], v[66:69]
	v_mfma_f32_16x16x128_f8f6f4 v[46:49], v[26:33], v[200:207], v[46:49]
	v_mfma_f32_16x16x128_f8f6f4 v[50:53], v[18:25], v[200:207], v[50:53]
	s_setprio 0
	s_barrier
	s_movk_i32 s38, 0x100
	s_andn2_b64 vcc, exec, s[34:35]
	s_mov_b64 s[36:37], -1
	s_mov_b64 s[34:35], 0
	s_cbranch_vccz .LBB0_1558
	s_and_b64 vcc, exec, s[12:13]
	s_cbranch_vccz .LBB0_1561
	s_barrier

.LBB0_1745:
	s_add_u32 s8, s49, s6
	s_addc_u32 s9, s50, s7
	s_add_u32 s8, s8, 0x32800100
	s_addc_u32 s9, s9, 0
	s_add_u32 s73, s51, s6
	s_addc_u32 s74, s54, s7
	s_add_i32 s72, 0, 0x10000
	s_cmpk_eq_i32 s6, 0x2a00
	s_cselect_b32 s37, s5, s9
	s_cselect_b32 s36, s4, s8
	s_cselect_b32 s9, s13, s74
	s_cselect_b32 s8, s12, s73
	s_add_i32 s73, 0, 0x14000
	v_add_u32_e32 v2, s72, v188
	v_add_u32_e32 v6, s73, v188
	ds_read_b128 v[26:29], v2
	ds_read_b128 v[30:33], v2 offset:1024
	ds_read_b128 v[18:21], v2 offset:2048
	ds_read_b128 v[22:25], v2 offset:3072
	ds_read_b128 v[10:13], v6
	ds_read_b128 v[14:17], v6 offset:1024
	ds_read_b128 v[2:5], v6 offset:2048
	ds_read_b128 v[6:9], v6 offset:3072
	v_lshl_add_u64 v[214:215], v[168:169], 0, s[6:7]
	s_add_i32 m0, s64, 0xc000
	ds_read_b128 v[172:175], v189
	ds_read_b128 v[176:179], v189 offset:1024
	ds_read_b128 v[190:193], v189 offset:2048
	ds_read_b128 v[194:197], v189 offset:3072
	ds_read_b128 v[198:201], v189 offset:4096
	ds_read_b128 v[202:205], v189 offset:5120
	ds_read_b128 v[206:209], v189 offset:6144
	ds_read_b128 v[210:213], v189 offset:7168
	global_load_lds_dwordx4 v[214:215], off
	v_lshl_add_u64 v[214:215], v[170:171], 0, s[6:7]
	s_add_i32 m0, s64, 0xe000
	s_nop 0
	global_load_lds_dwordx4 v[214:215], off
	s_waitcnt vmcnt(8)
	s_waitcnt lgkmcnt(0)
	s_barrier
	s_setprio 1
	v_mfma_f32_16x16x128_f8f6f4 v[158:161], v[26:33], v[172:179], v[158:161]
	v_mfma_f32_16x16x128_f8f6f4 v[154:157], v[18:25], v[172:179], v[154:157]
	v_mfma_f32_16x16x128_f8f6f4 v[118:121], v[18:25], v[190:197], v[118:121]
	v_mfma_f32_16x16x128_f8f6f4 v[122:125], v[26:33], v[190:197], v[122:125]
	v_mfma_f32_16x16x128_f8f6f4 v[126:129], v[26:33], v[198:205], v[126:129]
	v_mfma_f32_16x16x128_f8f6f4 v[114:117], v[18:25], v[198:205], v[114:117]
	v_mfma_f32_16x16x128_f8f6f4 v[106:109], v[18:25], v[206:213], v[106:109]
	v_mfma_f32_16x16x128_f8f6f4 v[110:113], v[26:33], v[206:213], v[110:113]
	v_mfma_f32_16x16x128_f8f6f4 v[102:105], v[10:17], v[206:213], v[102:105]
	v_mfma_f32_16x16x128_f8f6f4 v[98:101], v[2:9], v[206:213], v[98:101]
	v_mfma_f32_16x16x128_f8f6f4 v[146:149], v[2:9], v[172:179], v[146:149]
	v_mfma_f32_16x16x128_f8f6f4 v[150:153], v[10:17], v[172:179], v[150:153]
	v_mfma_f32_16x16x128_f8f6f4 v[142:145], v[10:17], v[190:197], v[142:145]
	v_mfma_f32_16x16x128_f8f6f4 v[138:141], v[2:9], v[190:197], v[138:141]
	v_mfma_f32_16x16x128_f8f6f4 v[130:133], v[2:9], v[198:205], v[130:133]
	v_mfma_f32_16x16x128_f8f6f4 v[134:137], v[10:17], v[198:205], v[134:137]
	s_setprio 0
	s_barrier
	s_add_i32 s72, s72, s43
	v_lshl_add_u64 v[172:173], s[8:9], 0, v[162:163]
	s_mov_b32 m0, s72
	ds_read_b128 v[190:193], v189 offset:16384
	ds_read_b128 v[194:197], v189 offset:17408
	ds_read_b128 v[198:201], v189 offset:18432
	ds_read_b128 v[202:205], v189 offset:19456
	ds_read_b128 v[206:209], v189 offset:20480
	ds_read_b128 v[210:213], v189 offset:21504
	ds_read_b128 v[214:217], v189 offset:22528
	ds_read_b128 v[218:221], v189 offset:23552
	global_load_lds_dwordx4 v[172:173], off
	s_add_i32 m0, s72, 0x2000
	s_add_u32 s74, s8, 0x158000
	v_lshl_add_u64 v[174:175], s[8:9], 0, v[166:167]
	s_addc_u32 s75, s9, 0
	s_add_i32 s72, s73, s43
	global_load_lds_dwordx4 v[174:175], off
	s_mov_b32 m0, s72
	v_lshl_add_u64 v[178:179], s[36:37], 0, v[166:167]
	global_load_lds_dwordx4 v162, s[74:75]
	s_add_i32 m0, s72, 0x2000
	s_nop 0
	global_load_lds_dwordx4 v166, s[74:75]
	v_lshl_add_u64 v[176:177], s[36:37], 0, v[162:163]
	s_mov_b32 m0, s64
	s_nop 0
	global_load_lds_dwordx4 v[176:177], off
	s_mov_b32 m0, s65
	s_nop 0
	global_load_lds_dwordx4 v[178:179], off
	s_waitcnt vmcnt(8)
	s_waitcnt lgkmcnt(0)
	s_barrier
	s_setprio 1
	v_mfma_f32_16x16x128_f8f6f4 v[78:81], v[26:33], v[198:205], v[78:81]
	v_mfma_f32_16x16x128_f8f6f4 v[74:77], v[18:25], v[198:205], v[74:77]
	v_mfma_f32_16x16x128_f8f6f4 v[90:93], v[18:25], v[190:197], v[90:93]
	v_mfma_f32_16x16x128_f8f6f4 v[94:97], v[26:33], v[190:197], v[94:97]
	v_mfma_f32_16x16x128_f8f6f4 v[62:65], v[26:33], v[206:213], v[62:65]
	v_mfma_f32_16x16x128_f8f6f4 v[58:61], v[18:25], v[206:213], v[58:61]
	v_mfma_f32_16x16x128_f8f6f4 v[42:45], v[18:25], v[214:221], v[42:45]
	v_mfma_f32_16x16x128_f8f6f4 v[46:49], v[26:33], v[214:221], v[46:49]
	v_mfma_f32_16x16x128_f8f6f4 v[38:41], v[10:17], v[214:221], v[38:41]
	v_mfma_f32_16x16x128_f8f6f4 v[34:37], v[2:9], v[214:221], v[34:37]
	v_mfma_f32_16x16x128_f8f6f4 v[82:85], v[2:9], v[190:197], v[82:85]
	v_mfma_f32_16x16x128_f8f6f4 v[86:89], v[10:17], v[190:197], v[86:89]
	v_mfma_f32_16x16x128_f8f6f4 v[70:73], v[10:17], v[198:205], v[70:73]
	v_mfma_f32_16x16x128_f8f6f4 v[66:69], v[2:9], v[198:205], v[66:69]
	v_mfma_f32_16x16x128_f8f6f4 v[50:53], v[2:9], v[206:213], v[50:53]
	v_mfma_f32_16x16x128_f8f6f4 v[54:57], v[10:17], v[206:213], v[54:57]
	s_setprio 0
	s_barrier
	s_add_i32 s72, 0, 0x18000
	s_add_i32 s73, 0, 0x1c000
	v_add_u32_e32 v14, s72, v188
	v_add_u32_e32 v30, s73, v188
	ds_read_b128 v[2:5], v14
	ds_read_b128 v[6:9], v14 offset:1024
	ds_read_b128 v[10:13], v14 offset:2048
	ds_read_b128 v[14:17], v14 offset:3072
	ds_read_b128 v[18:21], v30
	ds_read_b128 v[22:25], v30 offset:1024
	ds_read_b128 v[26:29], v30 offset:2048
	ds_read_b128 v[30:33], v30 offset:3072
	s_add_u32 s36, s36, 0x158000
	s_addc_u32 s37, s37, 0
	s_mov_b32 m0, s66
	ds_read_b128 v[190:193], v189 offset:32768
	ds_read_b128 v[194:197], v189 offset:33792
	ds_read_b128 v[198:201], v189 offset:34816
	ds_read_b128 v[202:205], v189 offset:35840
	ds_read_b128 v[206:209], v189 offset:36864
	ds_read_b128 v[210:213], v189 offset:37888
	ds_read_b128 v[214:217], v189 offset:38912
	ds_read_b128 v[218:221], v189 offset:39936
	global_load_lds_dwordx4 v162, s[36:37]
	s_mov_b32 m0, s67
	s_nop 0
	global_load_lds_dwordx4 v166, s[36:37]
	s_waitcnt vmcnt(8)
	s_waitcnt lgkmcnt(0)
	s_barrier
	s_setprio 1
	v_mfma_f32_16x16x128_f8f6f4 v[114:117], v[10:17], v[206:213], v[114:117]
	v_mfma_f32_16x16x128_f8f6f4 v[126:129], v[2:9], v[206:213], v[126:129]
	v_mfma_f32_16x16x128_f8f6f4 v[158:161], v[2:9], v[190:197], v[158:161]
	v_mfma_f32_16x16x128_f8f6f4 v[154:157], v[10:17], v[190:197], v[154:157]
	v_mfma_f32_16x16x128_f8f6f4 v[118:121], v[10:17], v[198:205], v[118:121]
	v_mfma_f32_16x16x128_f8f6f4 v[122:125], v[2:9], v[198:205], v[122:125]
	v_mfma_f32_16x16x128_f8f6f4 v[110:113], v[2:9], v[214:221], v[110:113]
	v_mfma_f32_16x16x128_f8f6f4 v[106:109], v[10:17], v[214:221], v[106:109]
	v_mfma_f32_16x16x128_f8f6f4 v[102:105], v[18:25], v[214:221], v[102:105]
	v_mfma_f32_16x16x128_f8f6f4 v[98:101], v[26:33], v[214:221], v[98:101]
	v_mfma_f32_16x16x128_f8f6f4 v[146:149], v[26:33], v[190:197], v[146:149]
	v_mfma_f32_16x16x128_f8f6f4 v[150:153], v[18:25], v[190:197], v[150:153]
	v_mfma_f32_16x16x128_f8f6f4 v[142:145], v[18:25], v[198:205], v[142:145]
	v_mfma_f32_16x16x128_f8f6f4 v[138:141], v[26:33], v[198:205], v[138:141]
	v_mfma_f32_16x16x128_f8f6f4 v[130:133], v[26:33], v[206:213], v[130:133]
	v_mfma_f32_16x16x128_f8f6f4 v[134:137], v[18:25], v[206:213], v[134:137]
	s_setprio 0
	s_barrier
	s_add_i32 s36, s72, s43
	v_lshl_add_u64 v[172:173], v[172:173], 0, s[22:23]
	s_mov_b32 m0, s36
	ds_read_b128 v[190:193], v189 offset:49152
	ds_read_b128 v[194:197], v189 offset:50176
	ds_read_b128 v[198:201], v189 offset:51200
	ds_read_b128 v[202:205], v189 offset:52224
	ds_read_b128 v[206:209], v189 offset:53248
	ds_read_b128 v[210:213], v189 offset:54272
	ds_read_b128 v[214:217], v189 offset:55296
	ds_read_b128 v[218:221], v189 offset:56320
	global_load_lds_dwordx4 v[172:173], off
	s_add_i32 m0, s36, 0x2000
	s_add_u32 s8, s8, 0x158080
	v_lshl_add_u64 v[172:173], v[174:175], 0, s[22:23]
	s_addc_u32 s9, s9, 0
	s_add_i32 s36, s73, s43
	global_load_lds_dwordx4 v[172:173], off
	s_mov_b32 m0, s36
	s_nop 0
	global_load_lds_dwordx4 v162, s[8:9]
	s_add_i32 m0, s36, 0x2000
	s_nop 0
	global_load_lds_dwordx4 v166, s[8:9]
	v_lshl_add_u64 v[172:173], v[176:177], 0, s[22:23]
	s_mov_b32 m0, s69
	s_nop 0
	global_load_lds_dwordx4 v[172:173], off
	v_lshl_add_u64 v[172:173], v[178:179], 0, s[22:23]
	s_mov_b32 m0, s70
	s_nop 0
	global_load_lds_dwordx4 v[172:173], off
	s_waitcnt vmcnt(8)
	s_waitcnt lgkmcnt(0)
	s_barrier
	s_setprio 1
	v_mfma_f32_16x16x128_f8f6f4 v[62:65], v[2:9], v[206:213], v[62:65]
	v_mfma_f32_16x16x128_f8f6f4 v[58:61], v[10:17], v[206:213], v[58:61]
	v_mfma_f32_16x16x128_f8f6f4 v[90:93], v[10:17], v[190:197], v[90:93]
	v_mfma_f32_16x16x128_f8f6f4 v[94:97], v[2:9], v[190:197], v[94:97]
	v_mfma_f32_16x16x128_f8f6f4 v[78:81], v[2:9], v[198:205], v[78:81]
	v_mfma_f32_16x16x128_f8f6f4 v[74:77], v[10:17], v[198:205], v[74:77]
	v_mfma_f32_16x16x128_f8f6f4 v[42:45], v[10:17], v[214:221], v[42:45]
	v_mfma_f32_16x16x128_f8f6f4 v[46:49], v[2:9], v[214:221], v[46:49]
	v_mfma_f32_16x16x128_f8f6f4 v[38:41], v[18:25], v[214:221], v[38:41]
	v_mfma_f32_16x16x128_f8f6f4 v[34:37], v[26:33], v[214:221], v[34:37]
	v_mfma_f32_16x16x128_f8f6f4 v[82:85], v[26:33], v[190:197], v[82:85]
	v_mfma_f32_16x16x128_f8f6f4 v[86:89], v[18:25], v[190:197], v[86:89]
	v_mfma_f32_16x16x128_f8f6f4 v[70:73], v[18:25], v[198:205], v[70:73]
	v_mfma_f32_16x16x128_f8f6f4 v[66:69], v[26:33], v[198:205], v[66:69]
	v_mfma_f32_16x16x128_f8f6f4 v[50:53], v[26:33], v[206:213], v[50:53]
	v_mfma_f32_16x16x128_f8f6f4 v[54:57], v[18:25], v[206:213], v[54:57]
	s_setprio 0
	s_barrier
	s_add_i32 s71, s71, 2
	s_add_u32 s6, s6, 0x100
	s_addc_u32 s7, s7, 0
	s_cmpk_lt_u32 s71, 0x54
	s_cbranch_scc1 .LBB0_1745
	s_waitcnt vmcnt(0)
	s_cmpk_gt_u32 s40, 0xff
	s_cbranch_scc1 .LBB0_1748
	s_barrier

.LBB0_1807:
	ds_read_b128 v[26:29], v185
	ds_read_b128 v[30:33], v185 offset:1024
	ds_read_b128 v[18:21], v185 offset:2048
	ds_read_b128 v[22:25], v185 offset:3072
	ds_read_b128 v[10:13], v186
	ds_read_b128 v[14:17], v186 offset:1024
	ds_read_b128 v[2:5], v186 offset:2048
	ds_read_b128 v[6:9], v186 offset:3072
	s_add_u32 s28, s26, 0xffea8080
	s_addc_u32 s29, s27, -1
	s_cmpk_eq_i32 s58, 0x52
	s_cselect_b32 s31, s5, s29
	s_cselect_b32 s30, s4, s28
	s_cselect_b32 s29, s25, s57
	s_cselect_b32 s28, s24, s56
	s_add_i32 m0, s34, 0xc000
	ds_read_b128 v[174:177], v187
	ds_read_b128 v[178:181], v187 offset:1024
	ds_read_b128 v[188:191], v187 offset:2048
	ds_read_b128 v[192:195], v187 offset:3072
	ds_read_b128 v[196:199], v187 offset:4096
	ds_read_b128 v[200:203], v187 offset:5120
	ds_read_b128 v[204:207], v187 offset:6144
	ds_read_b128 v[208:211], v187 offset:7168
	global_load_lds_dwordx4 v166, s[26:27]
	v_lshl_add_u64 v[212:213], s[26:27], 0, v[168:169]
	s_add_i32 m0, s34, 0xe000
	s_nop 0
	global_load_lds_dwordx4 v[212:213], off
	s_waitcnt vmcnt(8)
	s_waitcnt lgkmcnt(0)
	s_barrier
	s_setprio 1
	v_mfma_f32_16x16x128_f8f6f4 v[158:161], v[26:33], v[174:181], v[158:161]
	v_mfma_f32_16x16x128_f8f6f4 v[154:157], v[18:25], v[174:181], v[154:157]
	v_mfma_f32_16x16x128_f8f6f4 v[138:141], v[18:25], v[188:195], v[138:141]
	v_mfma_f32_16x16x128_f8f6f4 v[142:145], v[26:33], v[188:195], v[142:145]
	v_mfma_f32_16x16x128_f8f6f4 v[126:129], v[26:33], v[196:203], v[126:129]
	v_mfma_f32_16x16x128_f8f6f4 v[122:125], v[18:25], v[196:203], v[122:125]
	v_mfma_f32_16x16x128_f8f6f4 v[106:109], v[18:25], v[204:211], v[106:109]
	v_mfma_f32_16x16x128_f8f6f4 v[110:113], v[26:33], v[204:211], v[110:113]
	v_mfma_f32_16x16x128_f8f6f4 v[102:105], v[10:17], v[204:211], v[102:105]
	v_mfma_f32_16x16x128_f8f6f4 v[98:101], v[2:9], v[204:211], v[98:101]
	v_mfma_f32_16x16x128_f8f6f4 v[146:149], v[2:9], v[174:181], v[146:149]
	v_mfma_f32_16x16x128_f8f6f4 v[150:153], v[10:17], v[174:181], v[150:153]
	v_mfma_f32_16x16x128_f8f6f4 v[134:137], v[10:17], v[188:195], v[134:137]
	v_mfma_f32_16x16x128_f8f6f4 v[130:133], v[2:9], v[188:195], v[130:133]
	v_mfma_f32_16x16x128_f8f6f4 v[114:117], v[2:9], v[196:203], v[114:117]
	v_mfma_f32_16x16x128_f8f6f4 v[118:121], v[10:17], v[196:203], v[118:121]
	s_setprio 0
	s_barrier
	s_add_i32 s59, s42, s3
	v_lshl_add_u64 v[174:175], s[28:29], 0, v[164:165]
	s_mov_b32 m0, s59
	ds_read_b128 v[188:191], v187 offset:16384
	ds_read_b128 v[192:195], v187 offset:17408
	ds_read_b128 v[196:199], v187 offset:18432
	ds_read_b128 v[200:203], v187 offset:19456
	ds_read_b128 v[204:207], v187 offset:20480
	ds_read_b128 v[208:211], v187 offset:21504
	ds_read_b128 v[212:215], v187 offset:22528
	ds_read_b128 v[216:219], v187 offset:23552
	global_load_lds_dwordx4 v[174:175], off
	s_add_i32 m0, s59, 0x2000
	s_add_u32 s60, s28, 0x158000
	v_lshl_add_u64 v[176:177], s[28:29], 0, v[162:163]
	s_addc_u32 s61, s29, 0
	s_add_i32 s59, s43, s3
	global_load_lds_dwordx4 v[176:177], off
	s_mov_b32 m0, s59
	v_lshl_add_u64 v[180:181], s[30:31], 0, v[162:163]
	global_load_lds_dwordx4 v164, s[60:61]
	s_add_i32 m0, s59, 0x2000
	s_nop 0
	global_load_lds_dwordx4 v162, s[60:61]
	v_lshl_add_u64 v[178:179], s[30:31], 0, v[164:165]
	s_mov_b32 m0, s34
	s_nop 0
	global_load_lds_dwordx4 v[178:179], off
	s_mov_b32 m0, s35
	s_nop 0
	global_load_lds_dwordx4 v[180:181], off
	s_waitcnt vmcnt(8)
	s_waitcnt lgkmcnt(0)
	s_barrier
	s_setprio 1
	v_mfma_f32_16x16x128_f8f6f4 v[78:81], v[26:33], v[196:203], v[78:81]
	v_mfma_f32_16x16x128_f8f6f4 v[74:77], v[18:25], v[196:203], v[74:77]
	v_mfma_f32_16x16x128_f8f6f4 v[90:93], v[18:25], v[188:195], v[90:93]
	v_mfma_f32_16x16x128_f8f6f4 v[94:97], v[26:33], v[188:195], v[94:97]
	v_mfma_f32_16x16x128_f8f6f4 v[62:65], v[26:33], v[204:211], v[62:65]
	v_mfma_f32_16x16x128_f8f6f4 v[58:61], v[18:25], v[204:211], v[58:61]
	v_mfma_f32_16x16x128_f8f6f4 v[42:45], v[18:25], v[212:219], v[42:45]
	v_mfma_f32_16x16x128_f8f6f4 v[54:57], v[26:33], v[212:219], v[54:57]
	v_mfma_f32_16x16x128_f8f6f4 v[38:41], v[10:17], v[212:219], v[38:41]
	v_mfma_f32_16x16x128_f8f6f4 v[34:37], v[2:9], v[212:219], v[34:37]
	v_mfma_f32_16x16x128_f8f6f4 v[82:85], v[2:9], v[188:195], v[82:85]
	v_mfma_f32_16x16x128_f8f6f4 v[86:89], v[10:17], v[188:195], v[86:89]
	v_mfma_f32_16x16x128_f8f6f4 v[70:73], v[10:17], v[196:203], v[70:73]
	v_mfma_f32_16x16x128_f8f6f4 v[66:69], v[2:9], v[196:203], v[66:69]
	v_mfma_f32_16x16x128_f8f6f4 v[46:49], v[2:9], v[204:211], v[46:49]
	v_mfma_f32_16x16x128_f8f6f4 v[50:53], v[10:17], v[204:211], v[50:53]
	s_setprio 0
	s_barrier
	s_add_i32 s59, 0, 0x18000
	s_add_i32 s60, 0, 0x1c000
	v_add_u32_e32 v14, s59, v183
	v_add_u32_e32 v30, s60, v183
	ds_read_b128 v[2:5], v14
	ds_read_b128 v[6:9], v14 offset:1024
	ds_read_b128 v[10:13], v14 offset:2048
	ds_read_b128 v[14:17], v14 offset:3072
	ds_read_b128 v[18:21], v30
	ds_read_b128 v[22:25], v30 offset:1024
	ds_read_b128 v[26:29], v30 offset:2048
	ds_read_b128 v[30:33], v30 offset:3072
	s_add_u32 s30, s30, 0x158000
	s_addc_u32 s31, s31, 0
	s_mov_b32 m0, s36
	ds_read_b128 v[188:191], v187 offset:32768
	ds_read_b128 v[192:195], v187 offset:33792
	ds_read_b128 v[196:199], v187 offset:34816
	ds_read_b128 v[200:203], v187 offset:35840
	ds_read_b128 v[204:207], v187 offset:36864
	ds_read_b128 v[208:211], v187 offset:37888
	ds_read_b128 v[212:215], v187 offset:38912
	ds_read_b128 v[216:219], v187 offset:39936
	global_load_lds_dwordx4 v164, s[30:31]
	s_mov_b32 m0, s37
	s_nop 0
	global_load_lds_dwordx4 v162, s[30:31]
	s_waitcnt vmcnt(8)
	s_waitcnt lgkmcnt(0)
	s_barrier
	s_setprio 1
	v_mfma_f32_16x16x128_f8f6f4 v[122:125], v[10:17], v[204:211], v[122:125]
	v_mfma_f32_16x16x128_f8f6f4 v[126:129], v[2:9], v[204:211], v[126:129]
	v_mfma_f32_16x16x128_f8f6f4 v[158:161], v[2:9], v[188:195], v[158:161]
	v_mfma_f32_16x16x128_f8f6f4 v[154:157], v[10:17], v[188:195], v[154:157]
	v_mfma_f32_16x16x128_f8f6f4 v[138:141], v[10:17], v[196:203], v[138:141]
	v_mfma_f32_16x16x128_f8f6f4 v[142:145], v[2:9], v[196:203], v[142:145]
	v_mfma_f32_16x16x128_f8f6f4 v[110:113], v[2:9], v[212:219], v[110:113]
	v_mfma_f32_16x16x128_f8f6f4 v[106:109], v[10:17], v[212:219], v[106:109]
	v_mfma_f32_16x16x128_f8f6f4 v[102:105], v[18:25], v[212:219], v[102:105]
	v_mfma_f32_16x16x128_f8f6f4 v[98:101], v[26:33], v[212:219], v[98:101]
	v_mfma_f32_16x16x128_f8f6f4 v[146:149], v[26:33], v[188:195], v[146:149]
	v_mfma_f32_16x16x128_f8f6f4 v[150:153], v[18:25], v[188:195], v[150:153]
	v_mfma_f32_16x16x128_f8f6f4 v[134:137], v[18:25], v[196:203], v[134:137]
	v_mfma_f32_16x16x128_f8f6f4 v[130:133], v[26:33], v[196:203], v[130:133]
	v_mfma_f32_16x16x128_f8f6f4 v[114:117], v[26:33], v[204:211], v[114:117]
	v_mfma_f32_16x16x128_f8f6f4 v[118:121], v[18:25], v[204:211], v[118:121]
	s_setprio 0
	s_barrier
	s_add_i32 s30, s59, s3
	v_lshl_add_u64 v[174:175], v[174:175], 0, s[10:11]
	s_mov_b32 m0, s30
	ds_read_b128 v[188:191], v187 offset:49152
	ds_read_b128 v[192:195], v187 offset:50176
	ds_read_b128 v[196:199], v187 offset:51200
	ds_read_b128 v[200:203], v187 offset:52224
	ds_read_b128 v[204:207], v187 offset:53248
	ds_read_b128 v[208:211], v187 offset:54272
	ds_read_b128 v[212:215], v187 offset:55296
	ds_read_b128 v[216:219], v187 offset:56320
	global_load_lds_dwordx4 v[174:175], off
	s_add_i32 m0, s30, 0x2000
	s_add_u32 s28, s28, 0x158080
	v_lshl_add_u64 v[174:175], v[176:177], 0, s[10:11]
	s_addc_u32 s29, s29, 0
	s_add_i32 s30, s60, s3
	global_load_lds_dwordx4 v[174:175], off
	s_mov_b32 m0, s30
	s_nop 0
	global_load_lds_dwordx4 v164, s[28:29]
	s_add_i32 m0, s30, 0x2000
	s_nop 0
	global_load_lds_dwordx4 v162, s[28:29]
	v_lshl_add_u64 v[174:175], v[178:179], 0, s[10:11]
	s_mov_b32 m0, s40
	s_nop 0
	global_load_lds_dwordx4 v[174:175], off
	v_lshl_add_u64 v[174:175], v[180:181], 0, s[10:11]
	s_mov_b32 m0, s41
	s_nop 0
	global_load_lds_dwordx4 v[174:175], off
	s_waitcnt vmcnt(8)
	s_waitcnt lgkmcnt(0)
	s_barrier
	s_setprio 1
	v_mfma_f32_16x16x128_f8f6f4 v[62:65], v[2:9], v[204:211], v[62:65]
	v_mfma_f32_16x16x128_f8f6f4 v[58:61], v[10:17], v[204:211], v[58:61]
	v_mfma_f32_16x16x128_f8f6f4 v[90:93], v[10:17], v[188:195], v[90:93]
	v_mfma_f32_16x16x128_f8f6f4 v[94:97], v[2:9], v[188:195], v[94:97]
	v_mfma_f32_16x16x128_f8f6f4 v[78:81], v[2:9], v[196:203], v[78:81]
	v_mfma_f32_16x16x128_f8f6f4 v[74:77], v[10:17], v[196:203], v[74:77]
	v_mfma_f32_16x16x128_f8f6f4 v[42:45], v[10:17], v[212:219], v[42:45]
	v_mfma_f32_16x16x128_f8f6f4 v[54:57], v[2:9], v[212:219], v[54:57]
	v_mfma_f32_16x16x128_f8f6f4 v[38:41], v[18:25], v[212:219], v[38:41]
	v_mfma_f32_16x16x128_f8f6f4 v[34:37], v[26:33], v[212:219], v[34:37]
	v_mfma_f32_16x16x128_f8f6f4 v[82:85], v[26:33], v[188:195], v[82:85]
	v_mfma_f32_16x16x128_f8f6f4 v[86:89], v[18:25], v[188:195], v[86:89]
	v_mfma_f32_16x16x128_f8f6f4 v[70:73], v[18:25], v[196:203], v[70:73]
	v_mfma_f32_16x16x128_f8f6f4 v[66:69], v[26:33], v[196:203], v[66:69]
	v_mfma_f32_16x16x128_f8f6f4 v[46:49], v[26:33], v[204:211], v[46:49]
	v_mfma_f32_16x16x128_f8f6f4 v[50:53], v[18:25], v[204:211], v[50:53]
	s_setprio 0
	s_barrier
	s_add_i32 s58, s58, 2
	s_add_u32 s26, s26, 0x100
	s_addc_u32 s27, s27, 0
	s_add_u32 s56, s56, 0x100
	s_addc_u32 s57, s57, 0
	s_cmpk_gt_u32 s58, 0x53
	s_cbranch_scc0 .LBB0_1807
	s_and_b64 vcc, exec, s[12:13]
	s_cbranch_vccz .LBB0_1810
	s_barrier
